# v32_wmove
# speedup vs baseline: 1.0648x; 1.0099x over previous
.LBB3_12:
	s_or_b64 exec, exec, s[20:21]
	v_mov_b32_e32 v107, v67
	ds_write_b128 v123, v[22:25] offset:35776
	ds_write_b128 v124, v[26:29] offset:40896
	ds_write_b128 v125, v[30:33] offset:46016
	ds_write_b128 v126, v[34:37] offset:51136
	ds_write_b128 v127, v[38:41] offset:56256
	v_lshl_add_u64 v[22:23], s[56:57], 0, v[106:107]
	v_add_co_u32_e32 v24, vcc, 0xc000, v22
	s_waitcnt lgkmcnt(0)
	s_nop 0
	v_addc_co_u32_e32 v25, vcc, 0, v23, vcc
	v_add_co_u32_e32 v28, vcc, 0xd000, v22
	s_barrier
	v_add_u32_e32 v196, 0x6f80, v129
	v_add_u32_e32 v197, 0x6f80, v123
	v_add_u32_e32 v198, 0x6f80, v124
	v_add_u32_e32 v199, 0x6f80, v125
	v_add_u32_e32 v200, 0x6f80, v126
	v_add_u32_e32 v201, 0x6f80, v127
	s_nop 0
	v_addc_co_u32_e32 v29, vcc, 0, v23, vcc
	v_add_co_u32_e32 v32, vcc, 0xf000, v22
	s_nop 1
	v_addc_co_u32_e32 v33, vcc, 0, v23, vcc
	v_add_co_u32_e32 v36, vcc, 0x10000, v22
	global_load_dwordx4 v[24:27], v[24:25], off offset:2048
	s_nop 0
	global_load_dwordx4 v[28:31], v[28:29], off offset:3072
	v_addc_co_u32_e32 v37, vcc, 0, v23, vcc
	v_add_co_u32_e32 v40, vcc, 0x11000, v22
	global_load_dwordx4 v[32:35], v[32:33], off
	s_nop 0
	global_load_dwordx4 v[36:39], v[36:37], off offset:1024
	v_addc_co_u32_e32 v41, vcc, 0, v23, vcc
	global_load_dwordx4 v[40:43], v[40:41], off offset:2048
	ds_write_b128 v197, v[2:5] offset:35776
	ds_write_b128 v198, v[6:9] offset:40896
	ds_write_b128 v199, v[10:13] offset:46016
	ds_write_b128 v200, v[14:17] offset:51136
	ds_write_b128 v201, v[18:21] offset:56256
	s_waitcnt vmcnt(5)
	ds_read_b128 v[44:47], v129 offset:35776
	ds_read_b128 v[48:51], v144
	ds_read_b128 v[52:55], v144 offset:64
	ds_read_b128 v[56:59], v129 offset:35840
	ds_read_b128 v[60:63], v129 offset:42432
	ds_read_b128 v[152:155], v129 offset:42496
	ds_read_b128 v[156:159], v129 offset:49088
	ds_read_b128 v[160:163], v129 offset:49152
	s_waitcnt lgkmcnt(6)
	v_mfma_f32_16x16x32_f16 v[44:47], v[44:47], v[48:51], 0
	ds_read_b128 v[164:167], v129 offset:55744
	ds_read_b128 v[168:171], v129 offset:55808
	s_waitcnt lgkmcnt(5)
	v_mfma_f32_16x16x32_f16 v[60:63], v[60:63], v[48:51], 0
	v_mfma_f32_16x16x32_f16 v[44:47], v[56:59], v[52:55], v[44:47]
	s_waitcnt lgkmcnt(4)
	v_mfma_f32_16x16x32_f16 v[56:59], v[152:155], v[52:55], v[60:63]
	ds_read_b128 v[152:155], v129 offset:35904
	s_waitcnt lgkmcnt(4)
	v_mfma_f32_16x16x32_f16 v[156:159], v[156:159], v[48:51], 0
	s_waitcnt lgkmcnt(2)
	v_mfma_f32_16x16x32_f16 v[48:51], v[164:167], v[48:51], 0
	v_mfma_f32_16x16x32_f16 v[60:63], v[160:163], v[52:55], v[156:159]
	s_waitcnt lgkmcnt(1)
	v_mfma_f32_16x16x32_f16 v[48:51], v[168:171], v[52:55], v[48:51]
	ds_read_b128 v[52:55], v144 offset:128
	s_nop 1
	ds_read_b128 v[156:159], v144 offset:192
	ds_read_b128 v[160:163], v129 offset:35968
	s_waitcnt lgkmcnt(2)
	v_mfma_f32_16x16x32_f16 v[44:47], v[152:155], v[52:55], v[44:47]
	ds_read_b128 v[152:155], v129 offset:42560
	ds_read_b128 v[164:167], v129 offset:42624
	s_waitcnt lgkmcnt(1)
	v_mfma_f32_16x16x32_f16 v[56:59], v[152:155], v[52:55], v[56:59]
	ds_read_b128 v[152:155], v129 offset:49216
	ds_read_b128 v[168:171], v129 offset:49280
	s_waitcnt lgkmcnt(1)
	v_mfma_f32_16x16x32_f16 v[60:63], v[152:155], v[52:55], v[60:63]
	ds_read_b128 v[152:155], v129 offset:55872
	ds_read_b128 v[172:175], v129 offset:55936
	s_waitcnt lgkmcnt(1)
	v_mfma_f32_16x16x32_f16 v[48:51], v[152:155], v[52:55], v[48:51]
	v_mfma_f32_16x16x32_f16 v[44:47], v[160:163], v[156:159], v[44:47]
	ds_read_b128 v[52:55], v144 offset:256
	ds_read_b128 v[152:155], v144 offset:320
	ds_read_b128 v[160:163], v129 offset:36032
	ds_read_b128 v[176:179], v129 offset:36096
	v_mfma_f32_16x16x32_f16 v[56:59], v[164:167], v[156:159], v[56:59]
	ds_read_b128 v[164:167], v129 offset:42688
	ds_read_b128 v[180:183], v129 offset:42752
	ds_read_b128 v[184:187], v129 offset:49344
	ds_read_b128 v[188:191], v129 offset:49408
	v_mfma_f32_16x16x32_f16 v[60:63], v[168:171], v[156:159], v[60:63]
	ds_read_b128 v[168:171], v129 offset:56000
	ds_read_b128 v[192:195], v129 offset:56064
	s_waitcnt lgkmcnt(0)
	v_mfma_f32_16x16x32_f16 v[48:51], v[172:175], v[156:159], v[48:51]
	v_add_co_u32_e32 v18, vcc, s75, v22
	v_mfma_f32_16x16x32_f16 v[2:5], v[160:163], v[52:55], v[44:47]
	s_nop 0
	v_addc_co_u32_e32 v19, vcc, 0, v23, vcc
	s_waitcnt lgkmcnt(0)
	v_add_co_u32_e32 v44, vcc, s76, v22
	v_mfma_f32_16x16x32_f16 v[14:17], v[168:171], v[52:55], v[48:51]
	s_nop 0
	v_addc_co_u32_e32 v45, vcc, 0, v23, vcc
	s_barrier
	v_add_co_u32_e32 v48, vcc, s77, v22
	v_mfma_f32_16x16x32_f16 v[6:9], v[164:167], v[52:55], v[56:59]
	s_nop 0
	v_addc_co_u32_e32 v49, vcc, 0, v23, vcc
	v_mfma_f32_16x16x32_f16 v[10:13], v[184:187], v[52:55], v[60:63]
	v_add_co_u32_e32 v52, vcc, s78, v22
	global_load_dwordx4 v[18:21], v[18:19], off offset:3072
	s_nop 0
	global_load_dwordx4 v[44:47], v[44:45], off
	v_addc_co_u32_e32 v53, vcc, 0, v23, vcc
	v_add_co_u32_e32 v56, vcc, s79, v22
	global_load_dwordx4 v[48:51], v[48:49], off offset:1024
	s_nop 0
	global_load_dwordx4 v[52:55], v[52:53], off offset:2048
	v_addc_co_u32_e32 v57, vcc, 0, v23, vcc
	global_load_dwordx4 v[56:59], v[56:57], off offset:3072
	s_waitcnt vmcnt(9)
	ds_write_b128 v123, v[24:27] offset:35776
	s_waitcnt vmcnt(8)
	ds_write_b128 v124, v[28:31] offset:40896
	s_waitcnt vmcnt(7)
	ds_write_b128 v125, v[32:35] offset:46016
	s_waitcnt vmcnt(6)
	ds_write_b128 v126, v[36:39] offset:51136
	s_waitcnt vmcnt(5)
	ds_write_b128 v127, v[40:43] offset:56256
	v_mfma_f32_16x16x32_f16 v[2:5], v[176:179], v[152:155], v[2:5]
	v_mfma_f32_16x16x32_f16 v[6:9], v[180:183], v[152:155], v[6:9]
	v_mfma_f32_16x16x32_f16 v[10:13], v[188:191], v[152:155], v[10:13]
	v_mfma_f32_16x16x32_f16 v[14:17], v[192:195], v[152:155], v[14:17]
	ds_read_b128 v[60:63], v196 offset:35776
	ds_read_b128 v[152:155], v144 offset:416
	ds_read_b128 v[156:159], v144 offset:480
	ds_read_b128 v[160:163], v196 offset:35840
	s_waitcnt lgkmcnt(2)
	v_mfma_f32_16x16x32_f16 v[2:5], v[60:63], v[152:155], v[2:5]
	ds_read_b128 v[60:63], v196 offset:42432
	ds_read_b128 v[164:167], v196 offset:42496
	s_waitcnt lgkmcnt(1)
	v_mfma_f32_16x16x32_f16 v[6:9], v[60:63], v[152:155], v[6:9]
	ds_read_b128 v[60:63], v196 offset:49088
	ds_read_b128 v[168:171], v196 offset:49152
	s_waitcnt lgkmcnt(1)
	v_mfma_f32_16x16x32_f16 v[10:13], v[60:63], v[152:155], v[10:13]
	ds_read_b128 v[60:63], v196 offset:55744
	ds_read_b128 v[172:175], v196 offset:55808
	s_waitcnt lgkmcnt(1)
	v_mfma_f32_16x16x32_f16 v[14:17], v[60:63], v[152:155], v[14:17]
	ds_read_b128 v[60:63], v196 offset:35904
	v_mfma_f32_16x16x32_f16 v[2:5], v[160:163], v[156:159], v[2:5]
	v_mfma_f32_16x16x32_f16 v[6:9], v[164:167], v[156:159], v[6:9]
	v_mfma_f32_16x16x32_f16 v[10:13], v[168:171], v[156:159], v[10:13]
	s_waitcnt lgkmcnt(1)
	v_mfma_f32_16x16x32_f16 v[14:17], v[172:175], v[156:159], v[14:17]
	ds_read_b128 v[152:155], v144 offset:544
	ds_read_b128 v[156:159], v144 offset:608
	ds_read_b128 v[160:163], v196 offset:35968
	s_waitcnt lgkmcnt(2)
	v_mfma_f32_16x16x32_f16 v[2:5], v[60:63], v[152:155], v[2:5]
	ds_read_b128 v[60:63], v196 offset:42560
	ds_read_b128 v[164:167], v196 offset:42624
	s_waitcnt lgkmcnt(1)
	v_mfma_f32_16x16x32_f16 v[6:9], v[60:63], v[152:155], v[6:9]
	ds_read_b128 v[60:63], v196 offset:49216
	ds_read_b128 v[168:171], v196 offset:49280
	s_waitcnt lgkmcnt(1)
	v_mfma_f32_16x16x32_f16 v[10:13], v[60:63], v[152:155], v[10:13]
	ds_read_b128 v[60:63], v196 offset:55872
	ds_read_b128 v[172:175], v196 offset:55936
	s_waitcnt lgkmcnt(1)
	v_mfma_f32_16x16x32_f16 v[14:17], v[60:63], v[152:155], v[14:17]
	v_mfma_f32_16x16x32_f16 v[2:5], v[160:163], v[156:159], v[2:5]
	ds_read_b128 v[60:63], v144 offset:672
	ds_read_b128 v[152:155], v144 offset:736
	ds_read_b128 v[160:163], v196 offset:36032
	ds_read_b128 v[176:179], v196 offset:36096
	v_mfma_f32_16x16x32_f16 v[6:9], v[164:167], v[156:159], v[6:9]
	ds_read_b128 v[164:167], v196 offset:42688
	ds_read_b128 v[180:183], v196 offset:42752
	ds_read_b128 v[184:187], v196 offset:49344
	ds_read_b128 v[188:191], v196 offset:49408
	v_mfma_f32_16x16x32_f16 v[10:13], v[168:171], v[156:159], v[10:13]
	ds_read_b128 v[168:171], v196 offset:56000
	ds_read_b128 v[192:195], v196 offset:56064
	s_waitcnt lgkmcnt(0)
	v_add_co_u32_e32 v24, vcc, s80, v22
	v_addc_co_u32_e32 v25, vcc, 0, v23, vcc
	v_add_co_u32_e32 v28, vcc, s81, v22
	s_waitcnt lgkmcnt(0)
	s_nop 0
	v_addc_co_u32_e32 v29, vcc, 0, v23, vcc
	v_add_co_u32_e32 v32, vcc, s82, v22
	s_barrier
	s_nop 0
	v_addc_co_u32_e32 v33, vcc, 0, v23, vcc
	v_add_co_u32_e32 v36, vcc, s83, v22
	s_nop 1
	v_addc_co_u32_e32 v37, vcc, 0, v23, vcc
	v_add_co_u32_e32 v40, vcc, s84, v22
	global_load_dwordx4 v[24:27], v[24:25], off
	s_nop 0
	global_load_dwordx4 v[28:31], v[28:29], off offset:1024
	s_nop 0
	global_load_dwordx4 v[32:35], v[32:33], off offset:2048
	s_nop 0
	global_load_dwordx4 v[36:39], v[36:37], off offset:3072
	v_addc_co_u32_e32 v41, vcc, 0, v23, vcc
	global_load_dwordx4 v[40:43], v[40:41], off
	s_waitcnt vmcnt(9)
	ds_write_b128 v197, v[18:21] offset:35776
	s_waitcnt vmcnt(8)
	ds_write_b128 v198, v[44:47] offset:40896
	s_waitcnt vmcnt(7)
	ds_write_b128 v199, v[48:51] offset:46016
	s_waitcnt vmcnt(6)
	ds_write_b128 v200, v[52:55] offset:51136
	s_waitcnt vmcnt(5)
	ds_write_b128 v201, v[56:59] offset:56256
	v_mfma_f32_16x16x32_f16 v[14:17], v[172:175], v[156:159], v[14:17]
	v_mfma_f32_16x16x32_f16 v[2:5], v[160:163], v[60:63], v[2:5]
	v_mfma_f32_16x16x32_f16 v[6:9], v[164:167], v[60:63], v[6:9]
	v_mfma_f32_16x16x32_f16 v[10:13], v[184:187], v[60:63], v[10:13]
	v_mfma_f32_16x16x32_f16 v[14:17], v[168:171], v[60:63], v[14:17]
	v_mfma_f32_16x16x32_f16 v[2:5], v[176:179], v[152:155], v[2:5]
	v_mfma_f32_16x16x32_f16 v[6:9], v[180:183], v[152:155], v[6:9]
	v_mfma_f32_16x16x32_f16 v[10:13], v[188:191], v[152:155], v[10:13]
	v_mfma_f32_16x16x32_f16 v[14:17], v[192:195], v[152:155], v[14:17]
	ds_read_b128 v[60:63], v129 offset:35776
	ds_read_b128 v[152:155], v144 offset:832
	ds_read_b128 v[156:159], v144 offset:896
	ds_read_b128 v[160:163], v129 offset:35840
	s_waitcnt lgkmcnt(2)
	v_mfma_f32_16x16x32_f16 v[2:5], v[60:63], v[152:155], v[2:5]
	ds_read_b128 v[60:63], v129 offset:42432
	ds_read_b128 v[164:167], v129 offset:42496
	s_waitcnt lgkmcnt(1)
	v_mfma_f32_16x16x32_f16 v[6:9], v[60:63], v[152:155], v[6:9]
	ds_read_b128 v[60:63], v129 offset:49088
	ds_read_b128 v[168:171], v129 offset:49152
	s_waitcnt lgkmcnt(1)
	v_mfma_f32_16x16x32_f16 v[10:13], v[60:63], v[152:155], v[10:13]
	ds_read_b128 v[60:63], v129 offset:55744
	ds_read_b128 v[172:175], v129 offset:55808
	s_waitcnt lgkmcnt(1)
	v_mfma_f32_16x16x32_f16 v[14:17], v[60:63], v[152:155], v[14:17]
	ds_read_b128 v[60:63], v129 offset:35904
	v_mfma_f32_16x16x32_f16 v[2:5], v[160:163], v[156:159], v[2:5]
	v_mfma_f32_16x16x32_f16 v[6:9], v[164:167], v[156:159], v[6:9]
	v_mfma_f32_16x16x32_f16 v[10:13], v[168:171], v[156:159], v[10:13]
	s_waitcnt lgkmcnt(1)
	v_mfma_f32_16x16x32_f16 v[14:17], v[172:175], v[156:159], v[14:17]
	ds_read_b128 v[152:155], v144 offset:960
	ds_read_b128 v[156:159], v144 offset:1024
	ds_read_b128 v[160:163], v129 offset:35968
	s_waitcnt lgkmcnt(2)
	v_mfma_f32_16x16x32_f16 v[2:5], v[60:63], v[152:155], v[2:5]
	ds_read_b128 v[60:63], v129 offset:42560
	ds_read_b128 v[164:167], v129 offset:42624
	s_waitcnt lgkmcnt(1)
	v_mfma_f32_16x16x32_f16 v[6:9], v[60:63], v[152:155], v[6:9]
	ds_read_b128 v[60:63], v129 offset:49216
	ds_read_b128 v[168:171], v129 offset:49280
	s_waitcnt lgkmcnt(1)
	v_mfma_f32_16x16x32_f16 v[10:13], v[60:63], v[152:155], v[10:13]
	ds_read_b128 v[60:63], v129 offset:55872
	ds_read_b128 v[172:175], v129 offset:55936
	s_waitcnt lgkmcnt(1)
	v_mfma_f32_16x16x32_f16 v[14:17], v[60:63], v[152:155], v[14:17]
	v_mfma_f32_16x16x32_f16 v[2:5], v[160:163], v[156:159], v[2:5]
	ds_read_b128 v[60:63], v144 offset:1088
	ds_read_b128 v[152:155], v144 offset:1152
	ds_read_b128 v[160:163], v129 offset:36032
	ds_read_b128 v[176:179], v129 offset:36096
	v_mfma_f32_16x16x32_f16 v[6:9], v[164:167], v[156:159], v[6:9]
	ds_read_b128 v[164:167], v129 offset:42688
	ds_read_b128 v[180:183], v129 offset:42752
	ds_read_b128 v[184:187], v129 offset:49344
	ds_read_b128 v[188:191], v129 offset:49408
	v_mfma_f32_16x16x32_f16 v[10:13], v[168:171], v[156:159], v[10:13]
	ds_read_b128 v[168:171], v129 offset:56000
	ds_read_b128 v[192:195], v129 offset:56064
	s_waitcnt lgkmcnt(0)
	v_add_co_u32_e32 v18, vcc, s85, v22
	v_addc_co_u32_e32 v19, vcc, 0, v23, vcc
	v_add_co_u32_e32 v44, vcc, s27, v22
	s_waitcnt lgkmcnt(0)
	s_nop 0
	v_addc_co_u32_e32 v45, vcc, 0, v23, vcc
	v_add_co_u32_e32 v48, vcc, s86, v22
	s_barrier
	s_nop 0
	v_addc_co_u32_e32 v49, vcc, 0, v23, vcc
	v_add_co_u32_e32 v52, vcc, s87, v22
	s_nop 1
	v_addc_co_u32_e32 v53, vcc, 0, v23, vcc
	v_add_co_u32_e32 v56, vcc, s88, v22
	global_load_dwordx4 v[18:21], v[18:19], off offset:1024
	s_nop 0
	global_load_dwordx4 v[44:47], v[44:45], off offset:2048
	s_nop 0
	global_load_dwordx4 v[48:51], v[48:49], off offset:3072
	s_nop 0
	global_load_dwordx4 v[52:55], v[52:53], off
	v_addc_co_u32_e32 v57, vcc, 0, v23, vcc
	global_load_dwordx4 v[56:59], v[56:57], off offset:1024
	s_waitcnt vmcnt(9)
	ds_write_b128 v123, v[24:27] offset:35776
	s_waitcnt vmcnt(8)
	ds_write_b128 v124, v[28:31] offset:40896
	s_waitcnt vmcnt(7)
	ds_write_b128 v125, v[32:35] offset:46016
	s_waitcnt vmcnt(6)
	ds_write_b128 v126, v[36:39] offset:51136
	s_waitcnt vmcnt(5)
	ds_write_b128 v127, v[40:43] offset:56256
	v_mfma_f32_16x16x32_f16 v[14:17], v[172:175], v[156:159], v[14:17]
	v_mfma_f32_16x16x32_f16 v[2:5], v[160:163], v[60:63], v[2:5]
	v_mfma_f32_16x16x32_f16 v[6:9], v[164:167], v[60:63], v[6:9]
	v_mfma_f32_16x16x32_f16 v[10:13], v[184:187], v[60:63], v[10:13]
	v_mfma_f32_16x16x32_f16 v[14:17], v[168:171], v[60:63], v[14:17]
	v_mfma_f32_16x16x32_f16 v[2:5], v[176:179], v[152:155], v[2:5]
	v_mfma_f32_16x16x32_f16 v[6:9], v[180:183], v[152:155], v[6:9]
	v_mfma_f32_16x16x32_f16 v[10:13], v[188:191], v[152:155], v[10:13]
	v_mfma_f32_16x16x32_f16 v[14:17], v[192:195], v[152:155], v[14:17]
	ds_read_b128 v[60:63], v196 offset:35776
	ds_read_b128 v[152:155], v144 offset:1248
	ds_read_b128 v[156:159], v144 offset:1312
	ds_read_b128 v[160:163], v196 offset:35840
	s_waitcnt lgkmcnt(2)
	v_mfma_f32_16x16x32_f16 v[2:5], v[60:63], v[152:155], v[2:5]
	ds_read_b128 v[60:63], v196 offset:42432
	ds_read_b128 v[164:167], v196 offset:42496
	s_waitcnt lgkmcnt(1)
	v_mfma_f32_16x16x32_f16 v[6:9], v[60:63], v[152:155], v[6:9]
	ds_read_b128 v[60:63], v196 offset:49088
	ds_read_b128 v[168:171], v196 offset:49152
	s_waitcnt lgkmcnt(1)
	v_mfma_f32_16x16x32_f16 v[10:13], v[60:63], v[152:155], v[10:13]
	ds_read_b128 v[60:63], v196 offset:55744
	ds_read_b128 v[172:175], v196 offset:55808
	s_waitcnt lgkmcnt(1)
	v_mfma_f32_16x16x32_f16 v[14:17], v[60:63], v[152:155], v[14:17]
	ds_read_b128 v[60:63], v196 offset:35904
	v_mfma_f32_16x16x32_f16 v[2:5], v[160:163], v[156:159], v[2:5]
	v_mfma_f32_16x16x32_f16 v[6:9], v[164:167], v[156:159], v[6:9]
	v_mfma_f32_16x16x32_f16 v[10:13], v[168:171], v[156:159], v[10:13]
	s_waitcnt lgkmcnt(1)
	v_mfma_f32_16x16x32_f16 v[14:17], v[172:175], v[156:159], v[14:17]
	ds_read_b128 v[152:155], v144 offset:1376
	ds_read_b128 v[156:159], v144 offset:1440
	ds_read_b128 v[160:163], v196 offset:35968
	s_waitcnt lgkmcnt(2)
	v_mfma_f32_16x16x32_f16 v[2:5], v[60:63], v[152:155], v[2:5]
	ds_read_b128 v[60:63], v196 offset:42560
	ds_read_b128 v[164:167], v196 offset:42624
	s_waitcnt lgkmcnt(1)
	v_mfma_f32_16x16x32_f16 v[6:9], v[60:63], v[152:155], v[6:9]
	ds_read_b128 v[60:63], v196 offset:49216
	ds_read_b128 v[168:171], v196 offset:49280
	s_waitcnt lgkmcnt(1)
	v_mfma_f32_16x16x32_f16 v[10:13], v[60:63], v[152:155], v[10:13]
	ds_read_b128 v[60:63], v196 offset:55872
	ds_read_b128 v[172:175], v196 offset:55936
	s_waitcnt lgkmcnt(1)
	v_mfma_f32_16x16x32_f16 v[14:17], v[60:63], v[152:155], v[14:17]
	v_mfma_f32_16x16x32_f16 v[2:5], v[160:163], v[156:159], v[2:5]
	ds_read_b128 v[60:63], v144 offset:1504
	ds_read_b128 v[152:155], v144 offset:1568
	ds_read_b128 v[160:163], v196 offset:36032
	ds_read_b128 v[176:179], v196 offset:36096
	v_mfma_f32_16x16x32_f16 v[6:9], v[164:167], v[156:159], v[6:9]
	ds_read_b128 v[164:167], v196 offset:42688
	ds_read_b128 v[180:183], v196 offset:42752
	ds_read_b128 v[184:187], v196 offset:49344
	ds_read_b128 v[188:191], v196 offset:49408
	v_mfma_f32_16x16x32_f16 v[10:13], v[168:171], v[156:159], v[10:13]
	ds_read_b128 v[168:171], v196 offset:56000
	ds_read_b128 v[192:195], v196 offset:56064
	s_waitcnt lgkmcnt(0)
	v_add_co_u32_e32 v24, vcc, s89, v22
	v_addc_co_u32_e32 v25, vcc, 0, v23, vcc
	v_add_co_u32_e32 v28, vcc, s90, v22
	s_waitcnt lgkmcnt(0)
	s_nop 0
	v_addc_co_u32_e32 v29, vcc, 0, v23, vcc
	v_add_co_u32_e32 v32, vcc, s91, v22
	s_barrier
	s_nop 0
	v_addc_co_u32_e32 v33, vcc, 0, v23, vcc
	v_add_co_u32_e32 v36, vcc, s92, v22
	s_nop 1
	v_addc_co_u32_e32 v37, vcc, 0, v23, vcc
	v_add_co_u32_e32 v22, vcc, s93, v22
	global_load_dwordx4 v[24:27], v[24:25], off offset:2048
	s_nop 0
	global_load_dwordx4 v[28:31], v[28:29], off offset:3072
	s_nop 0
	global_load_dwordx4 v[32:35], v[32:33], off
	s_nop 0
	global_load_dwordx4 v[36:39], v[36:37], off offset:1024
	v_addc_co_u32_e32 v23, vcc, 0, v23, vcc
	global_load_dwordx4 v[40:43], v[22:23], off offset:2048
	s_waitcnt vmcnt(9)
	ds_write_b128 v197, v[18:21] offset:35776
	s_waitcnt vmcnt(8)
	ds_write_b128 v198, v[44:47] offset:40896
	s_waitcnt vmcnt(7)
	ds_write_b128 v199, v[48:51] offset:46016
	s_waitcnt vmcnt(6)
	ds_write_b128 v200, v[52:55] offset:51136
	s_waitcnt vmcnt(5)
	ds_write_b128 v201, v[56:59] offset:56256
	v_mfma_f32_16x16x32_f16 v[14:17], v[172:175], v[156:159], v[14:17]
	v_mfma_f32_16x16x32_f16 v[2:5], v[160:163], v[60:63], v[2:5]
	v_mfma_f32_16x16x32_f16 v[6:9], v[164:167], v[60:63], v[6:9]
	v_mfma_f32_16x16x32_f16 v[10:13], v[184:187], v[60:63], v[10:13]
	v_mfma_f32_16x16x32_f16 v[14:17], v[168:171], v[60:63], v[14:17]
	v_mfma_f32_16x16x32_f16 v[2:5], v[176:179], v[152:155], v[2:5]
	v_mfma_f32_16x16x32_f16 v[6:9], v[180:183], v[152:155], v[6:9]
	v_mfma_f32_16x16x32_f16 v[10:13], v[188:191], v[152:155], v[10:13]
	v_mfma_f32_16x16x32_f16 v[14:17], v[192:195], v[152:155], v[14:17]
	ds_read_b128 v[60:63], v129 offset:35776
	ds_read_b128 v[152:155], v144 offset:1664
	ds_read_b128 v[156:159], v144 offset:1728
	ds_read_b128 v[160:163], v129 offset:35840
	s_waitcnt lgkmcnt(2)
	v_mfma_f32_16x16x32_f16 v[2:5], v[60:63], v[152:155], v[2:5]
	ds_read_b128 v[60:63], v129 offset:42432
	ds_read_b128 v[164:167], v129 offset:42496
	s_waitcnt lgkmcnt(1)
	v_mfma_f32_16x16x32_f16 v[6:9], v[60:63], v[152:155], v[6:9]
	ds_read_b128 v[60:63], v129 offset:49088
	ds_read_b128 v[168:171], v129 offset:49152
	s_waitcnt lgkmcnt(1)
	v_mfma_f32_16x16x32_f16 v[10:13], v[60:63], v[152:155], v[10:13]
	ds_read_b128 v[60:63], v129 offset:55744
	ds_read_b128 v[172:175], v129 offset:55808
	s_waitcnt lgkmcnt(1)
	v_mfma_f32_16x16x32_f16 v[14:17], v[60:63], v[152:155], v[14:17]
	ds_read_b128 v[60:63], v129 offset:35904
	v_mfma_f32_16x16x32_f16 v[2:5], v[160:163], v[156:159], v[2:5]
	v_mfma_f32_16x16x32_f16 v[6:9], v[164:167], v[156:159], v[6:9]
	v_mfma_f32_16x16x32_f16 v[10:13], v[168:171], v[156:159], v[10:13]
	s_waitcnt lgkmcnt(1)
	v_mfma_f32_16x16x32_f16 v[14:17], v[172:175], v[156:159], v[14:17]
	ds_read_b128 v[152:155], v144 offset:1792
	ds_read_b128 v[156:159], v144 offset:1856
	ds_read_b128 v[160:163], v129 offset:35968
	s_waitcnt lgkmcnt(2)
	v_mfma_f32_16x16x32_f16 v[2:5], v[60:63], v[152:155], v[2:5]
	ds_read_b128 v[60:63], v129 offset:42560
	ds_read_b128 v[164:167], v129 offset:42624
	s_waitcnt lgkmcnt(1)
	v_mfma_f32_16x16x32_f16 v[6:9], v[60:63], v[152:155], v[6:9]
	ds_read_b128 v[60:63], v129 offset:49216
	ds_read_b128 v[168:171], v129 offset:49280
	s_waitcnt lgkmcnt(1)
	v_mfma_f32_16x16x32_f16 v[10:13], v[60:63], v[152:155], v[10:13]
	ds_read_b128 v[60:63], v129 offset:55872
	ds_read_b128 v[172:175], v129 offset:55936
	s_waitcnt lgkmcnt(1)
	v_mfma_f32_16x16x32_f16 v[14:17], v[60:63], v[152:155], v[14:17]
	ds_read_b128 v[60:63], v129 offset:36032
	v_mfma_f32_16x16x32_f16 v[2:5], v[160:163], v[156:159], v[2:5]
	v_mfma_f32_16x16x32_f16 v[6:9], v[164:167], v[156:159], v[6:9]
	v_mfma_f32_16x16x32_f16 v[10:13], v[168:171], v[156:159], v[10:13]
	s_waitcnt lgkmcnt(1)
	v_mfma_f32_16x16x32_f16 v[14:17], v[172:175], v[156:159], v[14:17]
	ds_read_b128 v[152:155], v144 offset:1920
	ds_read_b128 v[156:159], v144 offset:1984
	ds_read_b128 v[160:163], v129 offset:36096
	s_waitcnt lgkmcnt(2)
	v_mfma_f32_16x16x32_f16 v[2:5], v[60:63], v[152:155], v[2:5]
	ds_read_b128 v[60:63], v129 offset:42688
	ds_read_b128 v[164:167], v129 offset:42752
	s_waitcnt lgkmcnt(1)
	v_mfma_f32_16x16x32_f16 v[6:9], v[60:63], v[152:155], v[6:9]
	ds_read_b128 v[60:63], v129 offset:49344
	ds_read_b128 v[168:171], v129 offset:49408
	s_waitcnt lgkmcnt(1)
	v_mfma_f32_16x16x32_f16 v[10:13], v[60:63], v[152:155], v[10:13]
	ds_read_b128 v[60:63], v129 offset:56000
	ds_read_b128 v[172:175], v129 offset:56064
	s_waitcnt lgkmcnt(0)
	v_mfma_f32_16x16x32_f16 v[14:17], v[60:63], v[152:155], v[14:17]
	v_mfma_f32_16x16x32_f16 v[2:5], v[160:163], v[156:159], v[2:5]
	s_waitcnt lgkmcnt(0)
	s_barrier
	s_waitcnt vmcnt(4)
	ds_write_b128 v123, v[24:27] offset:35776
	s_waitcnt vmcnt(3)
	ds_write_b128 v124, v[28:31] offset:40896
	s_waitcnt vmcnt(2)
	ds_write_b128 v125, v[32:35] offset:46016
	s_waitcnt vmcnt(1)
	ds_write_b128 v126, v[36:39] offset:51136
	s_waitcnt vmcnt(0)
	ds_write_b128 v127, v[40:43] offset:56256
	v_mfma_f32_16x16x32_f16 v[6:9], v[164:167], v[156:159], v[6:9]
	v_mfma_f32_16x16x32_f16 v[10:13], v[168:171], v[156:159], v[10:13]
	v_mfma_f32_16x16x32_f16 v[14:17], v[172:175], v[156:159], v[14:17]
	ds_read_b128 v[18:21], v196 offset:35776
	ds_read_b128 v[44:47], v144 offset:2080
	ds_read_b128 v[48:51], v144 offset:2144
	ds_read_b128 v[52:55], v196 offset:35840
	s_waitcnt lgkmcnt(2)
	v_mfma_f32_16x16x32_f16 v[2:5], v[18:21], v[44:47], v[2:5]
	ds_read_b128 v[18:21], v196 offset:42432
	ds_read_b128 v[56:59], v196 offset:42496
	s_waitcnt lgkmcnt(1)
	v_mfma_f32_16x16x32_f16 v[6:9], v[18:21], v[44:47], v[6:9]
	ds_read_b128 v[18:21], v196 offset:49088
	ds_read_b128 v[60:63], v196 offset:49152
	s_waitcnt lgkmcnt(1)
	v_mfma_f32_16x16x32_f16 v[10:13], v[18:21], v[44:47], v[10:13]
	ds_read_b128 v[18:21], v196 offset:55744
	ds_read_b128 v[152:155], v196 offset:55808
	s_waitcnt lgkmcnt(1)
	v_mfma_f32_16x16x32_f16 v[14:17], v[18:21], v[44:47], v[14:17]
	ds_read_b128 v[18:21], v196 offset:35904
	v_mfma_f32_16x16x32_f16 v[2:5], v[52:55], v[48:51], v[2:5]
	v_mfma_f32_16x16x32_f16 v[6:9], v[56:59], v[48:51], v[6:9]
	v_mfma_f32_16x16x32_f16 v[10:13], v[60:63], v[48:51], v[10:13]
	s_waitcnt lgkmcnt(1)
	v_mfma_f32_16x16x32_f16 v[14:17], v[152:155], v[48:51], v[14:17]
	ds_read_b128 v[44:47], v144 offset:2208
	ds_read_b128 v[48:51], v144 offset:2272
	ds_read_b128 v[52:55], v196 offset:35968
	s_waitcnt lgkmcnt(2)
	v_mfma_f32_16x16x32_f16 v[2:5], v[18:21], v[44:47], v[2:5]
	ds_read_b128 v[18:21], v196 offset:42560
	ds_read_b128 v[56:59], v196 offset:42624
	s_waitcnt lgkmcnt(1)
	v_mfma_f32_16x16x32_f16 v[6:9], v[18:21], v[44:47], v[6:9]
	ds_read_b128 v[18:21], v196 offset:49216
	ds_read_b128 v[60:63], v196 offset:49280
	s_waitcnt lgkmcnt(1)
	v_mfma_f32_16x16x32_f16 v[10:13], v[18:21], v[44:47], v[10:13]
	ds_read_b128 v[18:21], v196 offset:55872
	ds_read_b128 v[152:155], v196 offset:55936
	s_waitcnt lgkmcnt(1)
	v_mfma_f32_16x16x32_f16 v[14:17], v[18:21], v[44:47], v[14:17]
	ds_read_b128 v[18:21], v196 offset:36032
	v_mfma_f32_16x16x32_f16 v[2:5], v[52:55], v[48:51], v[2:5]
	v_mfma_f32_16x16x32_f16 v[6:9], v[56:59], v[48:51], v[6:9]
	v_mfma_f32_16x16x32_f16 v[10:13], v[60:63], v[48:51], v[10:13]
	s_waitcnt lgkmcnt(1)
	v_mfma_f32_16x16x32_f16 v[14:17], v[152:155], v[48:51], v[14:17]
	ds_read_b128 v[44:47], v144 offset:2336
	ds_read_b128 v[48:51], v144 offset:2400
	ds_read_b128 v[52:55], v196 offset:36096
	s_waitcnt lgkmcnt(2)
	v_mfma_f32_16x16x32_f16 v[2:5], v[18:21], v[44:47], v[2:5]
	ds_read_b128 v[18:21], v196 offset:42688
	ds_read_b128 v[56:59], v196 offset:42752
	s_waitcnt lgkmcnt(1)
	v_mfma_f32_16x16x32_f16 v[6:9], v[18:21], v[44:47], v[6:9]
	ds_read_b128 v[18:21], v196 offset:49344
	ds_read_b128 v[60:63], v196 offset:49408
	s_waitcnt lgkmcnt(1)
	v_mfma_f32_16x16x32_f16 v[10:13], v[18:21], v[44:47], v[10:13]
	ds_read_b128 v[18:21], v196 offset:56000
	ds_read_b128 v[152:155], v196 offset:56064
	s_waitcnt lgkmcnt(0)
	v_mfma_f32_16x16x32_f16 v[14:17], v[18:21], v[44:47], v[14:17]
	v_mfma_f32_16x16x32_f16 v[2:5], v[52:55], v[48:51], v[2:5]
	s_waitcnt lgkmcnt(0)
	s_barrier
	v_mfma_f32_16x16x32_f16 v[6:9], v[56:59], v[48:51], v[6:9]
	v_mfma_f32_16x16x32_f16 v[10:13], v[60:63], v[48:51], v[10:13]
	v_mfma_f32_16x16x32_f16 v[14:17], v[152:155], v[48:51], v[14:17]
	ds_read_b128 v[18:21], v129 offset:35776
	ds_read_b128 v[22:25], v144 offset:2496
	ds_read_b128 v[26:29], v144 offset:2560
	ds_read_b128 v[30:33], v129 offset:35840
	s_waitcnt lgkmcnt(2)
	v_mfma_f32_16x16x32_f16 v[2:5], v[18:21], v[22:25], v[2:5]
	ds_read_b128 v[18:21], v129 offset:42432
	ds_read_b128 v[34:37], v129 offset:42496
	s_waitcnt lgkmcnt(1)
	v_mfma_f32_16x16x32_f16 v[6:9], v[18:21], v[22:25], v[6:9]
	ds_read_b128 v[18:21], v129 offset:49088
	ds_read_b128 v[38:41], v129 offset:49152
	s_waitcnt lgkmcnt(1)
	v_mfma_f32_16x16x32_f16 v[10:13], v[18:21], v[22:25], v[10:13]
	ds_read_b128 v[18:21], v129 offset:55744
	ds_read_b128 v[42:45], v129 offset:55808
	s_waitcnt lgkmcnt(1)
	v_mfma_f32_16x16x32_f16 v[14:17], v[18:21], v[22:25], v[14:17]
	v_mfma_f32_16x16x32_f16 v[2:5], v[30:33], v[26:29], v[2:5]
	ds_read_b128 v[18:21], v144 offset:2624
	ds_read_b128 v[22:25], v144 offset:2688
	ds_read_b128 v[30:33], v129 offset:35904
	ds_read_b128 v[46:49], v129 offset:35968
	s_waitcnt lgkmcnt(1)
	v_mfma_f32_16x16x32_f16 v[2:5], v[30:33], v[18:21], v[2:5]
	v_mfma_f32_16x16x32_f16 v[6:9], v[34:37], v[26:29], v[6:9]
	ds_read_b128 v[34:37], v129 offset:42560
	ds_read_b128 v[50:53], v129 offset:42624
	ds_read_b128 v[54:57], v129 offset:49216
	ds_read_b128 v[58:61], v129 offset:49280
	v_mfma_f32_16x16x32_f16 v[10:13], v[38:41], v[26:29], v[10:13]
	ds_read_b128 v[38:41], v129 offset:55872
	ds_read_b128 v[62:65], v129 offset:55936
	ds_read_b128 v[152:155], v129 offset:36032
	ds_read_b128 v[30:33], v144 offset:2752
	ds_read_b128 v[156:159], v144 offset:2816
	ds_read_b128 v[160:163], v129 offset:36096
	s_waitcnt lgkmcnt(10)
	v_mfma_f32_16x16x32_f16 v[2:5], v[46:49], v[22:25], v[2:5]
	ds_read_b128 v[46:49], v129 offset:42688
	ds_read_b128 v[164:167], v129 offset:42752
	ds_read_b128 v[168:171], v129 offset:49344
	ds_read_b128 v[172:175], v129 offset:49408
	s_waitcnt lgkmcnt(6)
	v_mfma_f32_16x16x32_f16 v[2:5], v[152:155], v[30:33], v[2:5]
	ds_read_b128 v[152:155], v129 offset:56000
	ds_read_b128 v[176:179], v129 offset:56064
	ds_read_b128 v[180:183], v98 offset:63808
	ds_read_b128 v[184:187], v98 offset:64064
	s_waitcnt lgkmcnt(8)
	v_mfma_f32_16x16x32_f16 v[2:5], v[160:163], v[156:159], v[2:5]
	ds_read_b128 v[160:163], v98 offset:63872
	ds_read_b128 v[188:191], v98 offset:64128
	v_mfma_f32_16x16x32_f16 v[14:17], v[42:45], v[26:29], v[14:17]
	s_waitcnt lgkmcnt(2)
	s_nop 3
	v_pk_fma_f32 v[2:3], v[2:3], v[180:181], v[184:185]
	s_nop 0
	v_pk_mul_f32 v[26:27], v[2:3], s[28:29] op_sel_hi:[1,0]
	v_mfma_f32_16x16x32_f16 v[6:9], v[34:37], v[18:21], v[6:9]
	v_mul_f32_e64 v29, |v26|, -|v26|
	v_mul_f32_e32 v29, 0x3fb8aa3b, v29
	v_fma_f32 v28, |v26|, s74, 1.0
	v_exp_f32_e32 v34, v29
	v_fma_f32 v29, |v27|, s74, 1.0
	v_rcp_f32_e32 v28, v28
	v_rcp_f32_e32 v29, v29
	v_mfma_f32_16x16x32_f16 v[10:13], v[54:57], v[18:21], v[10:13]
	v_mul_f32_e64 v35, |v27|, -|v27|
	v_mul_f32_e32 v35, 0x3fb8aa3b, v35
	v_exp_f32_e32 v35, v35
	v_mfma_f32_16x16x32_f16 v[16:19], v[38:41], v[18:21], v[14:17]
	v_mul_f32_e64 v2, v2, 0.5
	v_mul_f32_e64 v3, v3, 0.5
	s_nop 0
	v_mov_b64_e32 v[14:15], s[34:35]
	v_pk_fma_f32 v[20:21], v[28:29], s[40:41], v[14:15] op_sel_hi:[1,0,0]
	v_mfma_f32_16x16x32_f16 v[10:13], v[58:61], v[22:25], v[10:13]
	v_fma_f32 v20, v28, v20, s42
	v_fma_f32 v21, v29, v21, s42
	v_pk_fma_f32 v[20:21], v[28:29], v[20:21], s[44:45] op_sel_hi:[1,1,0]
	v_mfma_f32_16x16x32_f16 v[6:9], v[50:53], v[22:25], v[6:9]
	v_fma_f32 v20, v28, v20, s46
	v_fma_f32 v21, v29, v21, s46
	v_pk_mul_f32 v[20:21], v[20:21], v[28:29] neg_lo:[0,1] neg_hi:[0,1]
	v_mfma_f32_16x16x32_f16 v[16:19], v[62:65], v[22:25], v[16:19]
	v_fma_f32 v20, v20, v34, 1.0
	v_fma_f32 v21, v21, v35, 1.0
	v_bfi_b32 v21, s71, v21, v27
	v_bfi_b32 v20, s71, v20, v26
	v_pk_fma_f32 v[26:27], v[4:5], v[182:183], v[186:187]
	v_pk_add_f32 v[20:21], v[20:21], 1.0 op_sel_hi:[1,0]
	v_pk_mul_f32 v[28:29], v[26:27], s[28:29] op_sel_hi:[1,0]
	v_pk_mul_f32 v[24:25], v[2:3], v[20:21]
	v_mfma_f32_16x16x32_f16 v[2:5], v[168:171], v[30:33], v[10:13]
	v_mul_f32_e64 v26, v26, 0.5
	v_mul_f32_e64 v27, v27, 0.5
	s_nop 0
	v_fma_f32 v10, |v28|, s74, 1.0
	v_fma_f32 v11, |v29|, s74, 1.0
	v_rcp_f32_e32 v34, v10
	v_rcp_f32_e32 v35, v11
	v_mul_f32_e64 v10, |v28|, -|v28|
	v_mul_f32_e32 v10, 0x3fb8aa3b, v10
	v_mfma_f32_16x16x32_f16 v[6:9], v[46:49], v[30:33], v[6:9]
	v_mfma_f32_16x16x32_f16 v[16:19], v[152:155], v[30:33], v[16:19]
	v_exp_f32_e32 v30, v10
	v_mfma_f32_16x16x32_f16 v[10:13], v[172:175], v[156:159], v[2:5]
	s_nop 2
	v_mul_f32_e64 v4, |v29|, -|v29|
	v_pk_fma_f32 v[2:3], v[34:35], s[40:41], v[14:15] op_sel_hi:[1,0,0]
	v_mul_f32_e32 v4, 0x3fb8aa3b, v4
	v_pk_fma_f32 v[2:3], v[34:35], v[2:3], s[42:43] op_sel_hi:[1,1,0]
	v_exp_f32_e32 v31, v4
	v_pk_fma_f32 v[2:3], v[34:35], v[2:3], s[44:45] op_sel_hi:[1,1,0]
	v_mfma_f32_16x16x32_f16 v[20:23], v[164:167], v[156:159], v[6:9]
	v_fma_f32 v2, v34, v2, s46
	v_fma_f32 v3, v35, v3, s46
	v_pk_mul_f32 v[2:3], v[2:3], v[34:35] neg_lo:[0,1] neg_hi:[0,1]
	v_mfma_f32_16x16x32_f16 v[6:9], v[176:179], v[156:159], v[16:19]
	v_fma_f32 v2, v2, v30, 1.0
	v_fma_f32 v3, v3, v31, 1.0
	v_bfi_b32 v3, s71, v3, v29
	v_bfi_b32 v2, s71, v2, v28
	v_pk_add_f32 v[2:3], v[2:3], 1.0 op_sel_hi:[1,0]
	s_nop 0
	v_pk_mul_f32 v[4:5], v[26:27], v[2:3]
	v_cvt_pk_f16_f32 v2, v24, v25
	v_cvt_pk_f16_f32 v3, v4, v5
	s_waitcnt lgkmcnt(0)
	v_pk_fma_f32 v[4:5], v[20:21], v[160:161], v[188:189]
	s_nop 0
	v_pk_mul_f32 v[16:17], v[4:5], s[28:29] op_sel_hi:[1,0]
	v_pk_mul_f32 v[4:5], v[4:5], 0.5 op_sel_hi:[1,0]
	v_fma_f32 v18, |v16|, s74, 1.0
	v_fma_f32 v19, |v17|, s74, 1.0
	v_rcp_f32_e32 v18, v18
	v_rcp_f32_e32 v19, v19
	v_mul_f32_e64 v20, |v16|, -|v16|
	v_mul_f32_e64 v21, |v17|, -|v17|
	v_mul_f32_e32 v20, 0x3fb8aa3b, v20
	v_pk_fma_f32 v[24:25], v[18:19], s[40:41], v[14:15] op_sel_hi:[1,0,0]
	v_mul_f32_e32 v21, 0x3fb8aa3b, v21
	v_exp_f32_e32 v20, v20
	v_pk_fma_f32 v[24:25], v[18:19], v[24:25], s[42:43] op_sel_hi:[1,1,0]
	v_exp_f32_e32 v21, v21
	v_pk_fma_f32 v[24:25], v[18:19], v[24:25], s[44:45] op_sel_hi:[1,1,0]
	s_nop 0
	v_pk_fma_f32 v[24:25], v[18:19], v[24:25], s[46:47] op_sel_hi:[1,1,0]
	s_nop 0
	v_pk_mul_f32 v[18:19], v[24:25], v[18:19] neg_lo:[0,1] neg_hi:[0,1]
	s_nop 0
	v_pk_fma_f32 v[18:19], v[18:19], v[20:21], 1.0 op_sel_hi:[1,1,0]
	s_nop 0
	v_bfi_b32 v17, s71, v19, v17
	v_bfi_b32 v16, s71, v18, v16
	v_pk_add_f32 v[16:17], v[16:17], 1.0 op_sel_hi:[1,0]
	s_nop 0
	v_pk_mul_f32 v[4:5], v[4:5], v[16:17]
	v_pk_fma_f32 v[16:17], v[22:23], v[162:163], v[190:191]
	v_cvt_pk_f16_f32 v4, v4, v5
	v_pk_mul_f32 v[18:19], v[16:17], s[28:29] op_sel_hi:[1,0]
	v_pk_mul_f32 v[16:17], v[16:17], 0.5 op_sel_hi:[1,0]
	v_fma_f32 v20, |v18|, s74, 1.0
	v_fma_f32 v21, |v19|, s74, 1.0
	v_rcp_f32_e32 v20, v20
	v_rcp_f32_e32 v21, v21
	v_mul_f32_e64 v22, |v18|, -|v18|
	v_mul_f32_e64 v23, |v19|, -|v19|
	v_mul_f32_e32 v22, 0x3fb8aa3b, v22
	v_pk_fma_f32 v[24:25], v[20:21], s[40:41], v[14:15] op_sel_hi:[1,0,0]
	v_mul_f32_e32 v23, 0x3fb8aa3b, v23
	v_exp_f32_e32 v22, v22
	v_pk_fma_f32 v[24:25], v[20:21], v[24:25], s[42:43] op_sel_hi:[1,1,0]
	v_exp_f32_e32 v23, v23
	v_pk_fma_f32 v[24:25], v[20:21], v[24:25], s[44:45] op_sel_hi:[1,1,0]
	s_nop 0
	v_pk_fma_f32 v[24:25], v[20:21], v[24:25], s[46:47] op_sel_hi:[1,1,0]
	s_nop 0
	v_pk_mul_f32 v[20:21], v[24:25], v[20:21] neg_lo:[0,1] neg_hi:[0,1]
	s_nop 0
	v_pk_fma_f32 v[20:21], v[20:21], v[22:23], 1.0 op_sel_hi:[1,1,0]
	s_nop 0
	v_bfi_b32 v19, s71, v21, v19
	v_bfi_b32 v18, s71, v20, v18
	v_pk_add_f32 v[18:19], v[18:19], 1.0 op_sel_hi:[1,0]
	s_nop 0
	v_pk_mul_f32 v[16:17], v[16:17], v[18:19]
	ds_read_b128 v[18:21], v98 offset:63936
	ds_read_b128 v[22:25], v98 offset:64192
	v_cvt_pk_f16_f32 v5, v16, v17
	ds_read_b128 v[26:29], v98 offset:64000
	ds_read_b128 v[30:33], v98 offset:64256
	s_waitcnt lgkmcnt(2)
	v_pk_fma_f32 v[10:11], v[10:11], v[18:19], v[22:23]
	s_nop 0
	v_pk_mul_f32 v[22:23], v[10:11], s[28:29] op_sel_hi:[1,0]
	v_pk_fma_f32 v[12:13], v[12:13], v[20:21], v[24:25]
	v_fma_f32 v16, |v22|, s74, 1.0
	v_fma_f32 v17, |v23|, s74, 1.0
	v_rcp_f32_e32 v16, v16
	v_rcp_f32_e32 v17, v17
	v_mul_f32_e64 v18, |v22|, -|v22|
	v_mul_f32_e64 v19, |v23|, -|v23|
	v_mul_f32_e32 v18, 0x3fb8aa3b, v18
	v_pk_fma_f32 v[34:35], v[16:17], s[40:41], v[14:15] op_sel_hi:[1,0,0]
	v_mul_f32_e32 v19, 0x3fb8aa3b, v19
	v_exp_f32_e32 v18, v18
	v_pk_fma_f32 v[34:35], v[16:17], v[34:35], s[42:43] op_sel_hi:[1,1,0]
	v_exp_f32_e32 v19, v19
	v_pk_fma_f32 v[34:35], v[16:17], v[34:35], s[44:45] op_sel_hi:[1,1,0]
	v_pk_mul_f32 v[10:11], v[10:11], 0.5 op_sel_hi:[1,0]
	v_pk_fma_f32 v[34:35], v[16:17], v[34:35], s[46:47] op_sel_hi:[1,1,0]
	v_pk_mul_f32 v[20:21], v[12:13], s[28:29] op_sel_hi:[1,0]
	v_pk_mul_f32 v[16:17], v[34:35], v[16:17] neg_lo:[0,1] neg_hi:[0,1]
	v_mul_f32_e64 v24, |v20|, -|v20|
	v_pk_fma_f32 v[46:47], v[16:17], v[18:19], 1.0 op_sel_hi:[1,1,0]
	v_lshl_add_u64 v[18:19], s[50:51], 1, v[100:101]
	global_load_dwordx4 v[34:37], v[18:19], off
	global_load_dwordx4 v[42:45], v[18:19], off offset:1024
	v_lshl_add_u64 v[16:17], s[50:51], 2, v[102:103]
	global_load_dwordx4 v[38:41], v[16:17], off
	v_mov_b32_e32 v190, 0x1000
	v_mov_b32_e32 v191, 0
	global_load_dwordx4 v[152:155], v[18:19], off offset:2048
	global_load_dwordx4 v[156:159], v[18:19], off offset:3072
	global_load_dwordx4 v[160:163], v[16:17], off offset:64
	v_lshl_add_u64 v[188:189], v[18:19], 0, v[190:191]
	global_load_dwordx4 v[164:167], v[188:189], off
	global_load_dwordx4 v[168:171], v[188:189], off offset:1024
	global_load_dwordx4 v[172:175], v[16:17], off offset:128
	global_load_dwordx4 v[176:179], v[188:189], off offset:2048
	global_load_dwordx4 v[180:183], v[188:189], off offset:3072
	global_load_dwordx4 v[184:187], v[16:17], off offset:192
	v_bfi_b32 v23, s71, v47, v23
	v_bfi_b32 v22, s71, v46, v22
	v_pk_add_f32 v[22:23], v[22:23], 1.0 op_sel_hi:[1,0]
	v_mul_f32_e64 v25, |v21|, -|v21|
	v_pk_mul_f32 v[10:11], v[10:11], v[22:23]
	v_fma_f32 v22, |v20|, s74, 1.0
	v_fma_f32 v23, |v21|, s74, 1.0
	v_rcp_f32_e32 v22, v22
	v_rcp_f32_e32 v23, v23
	v_mul_f32_e32 v24, 0x3fb8aa3b, v24
	v_mul_f32_e32 v25, 0x3fb8aa3b, v25
	v_exp_f32_e32 v24, v24
	v_pk_fma_f32 v[46:47], v[22:23], s[40:41], v[14:15] op_sel_hi:[1,0,0]
	v_exp_f32_e32 v25, v25
	v_pk_fma_f32 v[46:47], v[22:23], v[46:47], s[42:43] op_sel_hi:[1,1,0]
	v_pk_mul_f32 v[12:13], v[12:13], 0.5 op_sel_hi:[1,0]
	v_pk_fma_f32 v[46:47], v[22:23], v[46:47], s[44:45] op_sel_hi:[1,1,0]
	s_waitcnt lgkmcnt(0)
	v_pk_fma_f32 v[6:7], v[6:7], v[26:27], v[30:31]
	v_pk_fma_f32 v[46:47], v[22:23], v[46:47], s[46:47] op_sel_hi:[1,1,0]
	v_cvt_pk_f16_f32 v10, v10, v11
	v_pk_mul_f32 v[22:23], v[46:47], v[22:23] neg_lo:[0,1] neg_hi:[0,1]
	v_pk_fma_f32 v[8:9], v[8:9], v[28:29], v[32:33]
	v_pk_fma_f32 v[22:23], v[22:23], v[24:25], 1.0 op_sel_hi:[1,1,0]
	s_mul_i32 s50, s94, 0xfef85000
	v_bfi_b32 v21, s71, v23, v21
	v_bfi_b32 v20, s71, v22, v20
	v_pk_add_f32 v[20:21], v[20:21], 1.0 op_sel_hi:[1,0]
	s_nop 0
	v_pk_mul_f32 v[12:13], v[12:13], v[20:21]
	s_nop 0
	v_cvt_pk_f16_f32 v11, v12, v13
	v_pk_mul_f32 v[12:13], v[6:7], s[28:29] op_sel_hi:[1,0]
	v_pk_mul_f32 v[6:7], v[6:7], 0.5 op_sel_hi:[1,0]
	v_fma_f32 v20, |v12|, s74, 1.0
	v_fma_f32 v21, |v13|, s74, 1.0
	v_rcp_f32_e32 v20, v20
	v_rcp_f32_e32 v21, v21
	v_mul_f32_e64 v22, |v12|, -|v12|
	v_mul_f32_e64 v23, |v13|, -|v13|
	v_mul_f32_e32 v22, 0x3fb8aa3b, v22
	v_pk_fma_f32 v[24:25], v[20:21], s[40:41], v[14:15] op_sel_hi:[1,0,0]
	v_mul_f32_e32 v23, 0x3fb8aa3b, v23
	v_exp_f32_e32 v22, v22
	v_pk_fma_f32 v[24:25], v[20:21], v[24:25], s[42:43] op_sel_hi:[1,1,0]
	v_exp_f32_e32 v23, v23
	v_pk_fma_f32 v[24:25], v[20:21], v[24:25], s[44:45] op_sel_hi:[1,1,0]
	s_nop 0
	v_pk_fma_f32 v[24:25], v[20:21], v[24:25], s[46:47] op_sel_hi:[1,1,0]
	s_nop 0
	v_pk_mul_f32 v[20:21], v[24:25], v[20:21] neg_lo:[0,1] neg_hi:[0,1]
	s_nop 0
	v_pk_fma_f32 v[20:21], v[20:21], v[22:23], 1.0 op_sel_hi:[1,1,0]
	s_nop 0
	v_bfi_b32 v13, s71, v21, v13
	v_bfi_b32 v12, s71, v20, v12
	v_pk_add_f32 v[12:13], v[12:13], 1.0 op_sel_hi:[1,0]
	s_nop 0
	v_pk_mul_f32 v[6:7], v[6:7], v[12:13]
	v_pk_mul_f32 v[12:13], v[8:9], s[28:29] op_sel_hi:[1,0]
	v_pk_mul_f32 v[8:9], v[8:9], 0.5 op_sel_hi:[1,0]
	v_fma_f32 v20, |v12|, s74, 1.0
	v_fma_f32 v21, |v13|, s74, 1.0
	v_rcp_f32_e32 v20, v20
	v_rcp_f32_e32 v21, v21
	v_mul_f32_e64 v22, |v12|, -|v12|
	v_mul_f32_e64 v23, |v13|, -|v13|
	v_mul_f32_e32 v22, 0x3fb8aa3b, v22
	v_pk_fma_f32 v[14:15], v[20:21], s[40:41], v[14:15] op_sel_hi:[1,0,0]
	v_mul_f32_e32 v23, 0x3fb8aa3b, v23
	v_exp_f32_e32 v22, v22
	v_pk_fma_f32 v[14:15], v[20:21], v[14:15], s[42:43] op_sel_hi:[1,1,0]
	v_exp_f32_e32 v23, v23
	v_pk_fma_f32 v[14:15], v[20:21], v[14:15], s[44:45] op_sel_hi:[1,1,0]
	s_nop 0
	v_pk_fma_f32 v[14:15], v[20:21], v[14:15], s[46:47] op_sel_hi:[1,1,0]
	s_nop 0
	v_pk_mul_f32 v[14:15], v[14:15], v[20:21] neg_lo:[0,1] neg_hi:[0,1]
	s_nop 0
	v_pk_fma_f32 v[14:15], v[14:15], v[22:23], 1.0 op_sel_hi:[1,1,0]
	s_nop 0
	v_bfi_b32 v13, s71, v15, v13
	v_bfi_b32 v12, s71, v14, v12
	v_pk_add_f32 v[12:13], v[12:13], 1.0 op_sel_hi:[1,0]
	v_add_u32_e32 v14, s95, v128
	v_pk_mul_f32 v[8:9], v[8:9], v[12:13]
	v_cvt_pk_f16_f32 v12, v6, v7
	v_cvt_pk_f16_f32 v13, v8, v9
	s_waitcnt vmcnt(0)
	v_pk_mul_f32 v[8:9], v[40:41], s[48:49] op_sel_hi:[1,0]
	v_pk_mul_f32 v[6:7], v[38:39], s[48:49] op_sel_hi:[1,0]
	v_cmp_gt_i32_e64 s[20:21], s73, v14
	v_add_u32_e32 v14, s50, v134
	v_mfma_f32_16x16x32_f16 v[6:9], v[34:37], v[2:5], v[6:9]
	v_mfma_f32_16x16x32_f16 v[6:9], v[42:45], v[10:13], v[6:9]
	v_pk_mul_f32 v[160:161], v[160:161], s[48:49] op_sel_hi:[1,0]
	v_pk_mul_f32 v[162:163], v[162:163], s[48:49] op_sel_hi:[1,0]
	v_pk_mul_f32 v[172:173], v[172:173], s[48:49] op_sel_hi:[1,0]
	v_pk_mul_f32 v[174:175], v[174:175], s[48:49] op_sel_hi:[1,0]
	v_pk_mul_f32 v[184:185], v[184:185], s[48:49] op_sel_hi:[1,0]
	v_pk_mul_f32 v[186:187], v[186:187], s[48:49] op_sel_hi:[1,0]
	s_nop 1
	v_mfma_f32_16x16x32_f16 v[20:23], v[152:155], v[2:5], v[160:163]
	v_mfma_f32_16x16x32_f16 v[24:27], v[164:167], v[2:5], v[172:175]
	v_mfma_f32_16x16x32_f16 v[28:31], v[176:179], v[2:5], v[184:187]
	v_mfma_f32_16x16x32_f16 v[20:23], v[156:159], v[10:13], v[20:23]
	v_mfma_f32_16x16x32_f16 v[24:27], v[168:171], v[10:13], v[24:27]
	v_mfma_f32_16x16x32_f16 v[28:31], v[180:183], v[10:13], v[28:31]
	s_and_saveexec_b64 s[50:51], s[20:21]
	s_cbranch_execz .Lmy_k2_nostore
	s_nop 7
	buffer_store_dwordx4 v[6:9], v14, s[24:27], 0 offen sc1
	buffer_store_dwordx4 v[20:23], v14, s[24:27], 0 offen offset:64 sc1
	buffer_store_dwordx4 v[24:27], v14, s[24:27], 0 offen offset:128 sc1
	buffer_store_dwordx4 v[28:31], v14, s[24:27], 0 offen offset:192 sc1

.LBB3_46:
	v_cmp_eq_u32_e32 vcc, 2, v3
	s_mov_b64 s[4:5], -1
	s_and_saveexec_b64 s[44:45], vcc
	s_cbranch_execz .LBB3_56
	v_lshrrev_b32_e32 v2, 2, v2
	v_and_b32_e32 v22, 12, v2
	v_mul_u32_u24_e32 v4, 48, v105
	v_or_b32_e32 v3, v22, v4
	v_lshlrev_b32_e32 v5, 2, v3
	v_or_b32_e32 v24, 3, v2
	v_or_b32_e32 v69, 19, v2
	v_or_b32_e32 v2, 35, v2
	v_or_b32_e32 v3, v24, v4
	v_add_lshl_u32 v26, v69, v4, 2
	v_add_lshl_u32 v4, v2, v4, 2
	v_add_u32_e32 v27, 0xc00, v5
	s_waitcnt lgkmcnt(0)
	global_load_dwordx3 v[6:8], v5, s[12:13]
	global_load_dwordx3 v[10:12], v5, s[14:15]
	v_lshlrev_b32_e32 v25, 2, v3
	global_load_dwordx3 v[14:16], v5, s[12:13] offset:64
	global_load_dwordx3 v[18:20], v5, s[14:15] offset:64
	global_load_dword v3, v25, s[12:13]
	global_load_dword v9, v25, s[14:15]
	global_load_dwordx3 v[32:34], v5, s[12:13] offset:128
	global_load_dwordx3 v[36:38], v5, s[14:15] offset:128
	global_load_dword v13, v26, s[12:13]
	global_load_dword v17, v26, s[14:15]
	global_load_dword v21, v4, s[12:13]
	global_load_dword v23, v4, s[14:15]
	global_load_dwordx3 v[40:42], v27, s[12:13] offset:64
	global_load_dwordx3 v[44:46], v27, s[14:15] offset:64
	global_load_dword v35, v26, s[12:13] offset:3072
	global_load_dword v39, v26, s[14:15] offset:3072
	global_load_dwordx3 v[48:50], v27, s[12:13] offset:128
	global_load_dwordx3 v[52:54], v27, s[14:15] offset:128
	v_mov_b32_e32 v26, 0x600
	v_mad_u32_u24 v73, v105, 48, v26
	global_load_dword v43, v4, s[12:13] offset:3072
	global_load_dword v47, v4, s[14:15] offset:3072
	global_load_dwordx2 v[74:75], v5, s[12:13] offset:3072
	global_load_dwordx2 v[76:77], v5, s[14:15] offset:3072
	global_load_dword v79, v25, s[12:13] offset:3072
	global_load_dword v81, v25, s[14:15] offset:3072
	global_load_dword v78, v27, s[12:13] offset:8
	global_load_dword v80, v27, s[14:15] offset:8
	v_or_b32_e32 v4, v22, v73
	v_lshlrev_b32_e32 v4, 2, v4
	v_add_lshl_u32 v2, v2, v73, 2
	global_load_dwordx3 v[56:58], v4, s[12:13] offset:128
	global_load_dwordx3 v[60:62], v4, s[14:15] offset:128
	global_load_dword v51, v2, s[12:13]
	global_load_dword v55, v2, s[14:15]
	global_load_dwordx3 v[66:68], v4, s[12:13]
	global_load_dwordx3 v[70:72], v4, s[14:15]
	v_or_b32_e32 v2, v24, v73
	v_lshlrev_b32_e32 v2, 2, v2
	global_load_dword v59, v2, s[12:13]
	global_load_dword v63, v2, s[14:15]
	global_load_dwordx3 v[28:30], v4, s[12:13] offset:64
	global_load_dwordx3 v[24:26], v4, s[14:15] offset:64
	v_lshl_or_b32 v31, v64, 4, v22
	v_cmp_eq_u32_e64 s[4:5], 3, v64
	s_mov_b32 s6, 0x4038aa3b
	s_mov_b32 s3, 0x3fb8aa3b
	v_cndmask_b32_e64 v2, v31, 0, s[4:5]
	v_lshlrev_b32_e32 v2, 2, v2
	global_load_dword v27, v2, s[24:25]
	s_mov_b32 s33, 0x3f2aaaab
	v_mov_b32_e32 v4, 0
	v_mov_b32_e32 v5, v4
	s_waitcnt vmcnt(36)
	v_mov_b32_e32 v2, v8
	s_waitcnt vmcnt(35)
	v_pk_mul_f32 v[6:7], v[6:7], v[10:11]
	v_mov_b32_e32 v8, v12
	s_waitcnt vmcnt(33)
	v_pk_mul_f32 v[10:11], v[14:15], v[18:19]
	v_mov_b32_e32 v12, v16
	v_mov_b32_e32 v16, v20
	s_waitcnt vmcnt(29)
	v_pk_mul_f32 v[14:15], v[32:33], v[36:37]
	v_mov_b32_e32 v20, v34
	v_mov_b32_e32 v22, v38
	v_pk_mul_f32 v[2:3], v[2:3], v[8:9]
	v_pk_mul_f32 v[8:9], v[10:11], s[6:7] op_sel_hi:[1,0]
	s_waitcnt vmcnt(27)
	v_pk_mul_f32 v[10:11], v[12:13], v[16:17]
	v_pk_mul_f32 v[12:13], v[14:15], s[6:7] op_sel_hi:[1,0]
	s_waitcnt vmcnt(25)
	v_pk_mul_f32 v[14:15], v[20:21], v[22:23]
	v_pk_mul_f32 v[16:17], v[2:3], s[6:7] op_sel_hi:[1,0]
	v_pk_mul_f32 v[10:11], v[10:11], s[6:7] op_sel_hi:[1,0]
	v_cvt_pk_f16_f32 v2, v12, v13
	v_pk_mul_f32 v[12:13], v[14:15], s[6:7] op_sel_hi:[1,0]
	s_waitcnt vmcnt(24)
	v_mov_b32_e32 v34, v42
	s_waitcnt vmcnt(23)
	v_mov_b32_e32 v38, v46
	s_waitcnt vmcnt(1)
	v_pk_mul_f32 v[24:25], v[28:29], v[24:25]
	v_or_b32_e32 v28, 1, v31
	v_cvt_pk_f16_f32 v8, v8, v9
	v_cvt_pk_f16_f32 v9, v10, v11
	v_cvt_pk_f16_f32 v3, v12, v13
	v_pk_mul_f32 v[10:11], v[40:41], v[44:45]
	v_pk_mul_f32 v[12:13], v[34:35], v[38:39]
	v_cndmask_b32_e64 v28, v28, 0, s[4:5]
	v_or_b32_e32 v29, 2, v31
	v_or_b32_e32 v31, 3, v31
	v_pk_mul_f32 v[10:11], v[10:11], s[6:7] op_sel_hi:[1,0]
	v_pk_mul_f32 v[12:13], v[12:13], s[6:7] op_sel_hi:[1,0]
	v_mov_b32_e32 v42, v50
	v_mov_b32_e32 v46, v54
	v_mov_b32_e32 v50, v58
	v_mov_b32_e32 v54, v62
	v_lshlrev_b32_e32 v28, 2, v28
	v_cndmask_b32_e64 v29, v29, 0, s[4:5]
	v_cndmask_b32_e64 v31, v31, 0, s[4:5]
	v_cvt_pk_f16_f32 v10, v10, v11
	v_cvt_pk_f16_f32 v11, v12, v13
	v_pk_mul_f32 v[12:13], v[48:49], v[52:53]
	v_pk_mul_f32 v[20:21], v[50:51], v[54:55]
	v_lshlrev_b32_e32 v29, 2, v29
	v_lshlrev_b32_e32 v31, 2, v31
	global_load_dword v50, v28, s[24:25]
	global_load_dword v52, v29, s[24:25]
	global_load_dword v54, v31, s[24:25]
	s_waitcnt vmcnt(3)
	v_mul_f32_e32 v28, 0x3fb8aa3b, v27
	v_fma_f32 v29, v27, s3, -v28
	v_rndne_f32_e32 v31, v28
	v_pk_mul_f32 v[14:15], v[42:43], v[46:47]
	v_fmac_f32_e32 v29, 0x32a5705f, v27
	v_sub_f32_e32 v28, v28, v31
	v_pk_mul_f32 v[12:13], v[12:13], s[6:7] op_sel_hi:[1,0]
	v_pk_mul_f32 v[14:15], v[14:15], s[6:7] op_sel_hi:[1,0]
	v_add_f32_e32 v28, v28, v29
	v_cvt_pk_f16_f32 v12, v12, v13
	v_cvt_pk_f16_f32 v13, v14, v15
	v_pk_mul_f32 v[14:15], v[74:75], v[76:77]
	v_exp_f32_e32 v28, v28
	v_cvt_i32_f32_e32 v29, v31
	v_pk_mul_f32 v[6:7], v[6:7], s[6:7] op_sel_hi:[1,0]
	v_pk_mul_f32 v[14:15], v[14:15], s[6:7] op_sel_hi:[1,0]
	v_mov_b32_e32 v58, v68
	v_mov_b32_e32 v62, v72
	v_cvt_pk_f16_f32 v6, v6, v7
	v_cvt_pk_f16_f32 v7, v16, v17
	v_cvt_pk_f16_f32 v16, v14, v15
	v_pk_mul_f32 v[14:15], v[78:79], v[80:81]
	v_pk_mul_f32 v[18:19], v[56:57], v[60:61]
	v_pk_mul_f32 v[22:23], v[66:67], v[70:71]
	v_pk_mul_f32 v[32:33], v[58:59], v[62:63]
	v_pk_mul_f32 v[24:25], v[24:25], s[6:7] op_sel_hi:[1,0]
	v_pk_mul_f32 v[14:15], v[14:15], s[6:7] op_sel_hi:[1,0]
	v_pk_mul_f32 v[18:19], v[18:19], s[6:7] op_sel_hi:[1,0]
	v_pk_mul_f32 v[20:21], v[20:21], s[6:7] op_sel_hi:[1,0]
	v_pk_mul_f32 v[22:23], v[22:23], s[6:7] op_sel_hi:[1,0]
	v_pk_mul_f32 v[32:33], v[32:33], s[6:7] op_sel_hi:[1,0]
	v_cvt_pk_f16_f32 v24, v24, v25
	v_add_lshl_u32 v25, v69, v73, 2
	s_mov_b32 s7, 0xc2ce8ed0
	v_cvt_pk_f16_f32 v22, v22, v23
	v_cvt_pk_f16_f32 v23, v32, v33
	global_load_dword v33, v25, s[12:13]
	global_load_dword v35, v25, s[14:15]
	v_ldexp_f32 v25, v28, v29
	v_cmp_ngt_f32_e32 vcc, s7, v27
	s_mov_b32 s12, 0x42b17218
	v_mov_b32_e32 v32, v30
	v_cndmask_b32_e32 v25, 0, v25, vcc
	v_mov_b32_e32 v30, 0x7f800000
	v_cmp_nlt_f32_e32 vcc, s12, v27
	v_mov_b32_e32 v55, 0x3ecc95a3
	s_mov_b32 s25, 0x3f317218
	v_cndmask_b32_e32 v25, v30, v25, vcc
	v_add_f32_e32 v27, 1.0, v25
	v_add_f32_e32 v28, -1.0, v27
	v_sub_f32_e32 v29, v28, v27
	v_add_f32_e32 v29, 1.0, v29
	v_sub_f32_e32 v28, v25, v28
	v_add_f32_e32 v31, v28, v29
	v_frexp_mant_f32_e32 v34, v27
	v_cvt_f64_f32_e32 v[28:29], v27
	v_frexp_exp_i32_f64_e32 v28, v[28:29]
	v_cmp_gt_f32_e32 vcc, s33, v34
	s_mov_b32 s13, 0x7f800000
	s_mov_b32 s15, 0x33800000
	v_subbrev_co_u32_e32 v34, vcc, 0, v28, vcc
	v_sub_u32_e32 v28, 0, v34
	v_ldexp_f32 v27, v27, v28
	v_ldexp_f32 v28, v31, v28
	v_add_f32_e32 v31, -1.0, v27
	v_add_f32_e32 v29, 1.0, v31
	v_sub_f32_e32 v29, v27, v29
	v_add_f32_e32 v36, v28, v29
	v_add_f32_e32 v29, 1.0, v27
	v_add_f32_e32 v37, -1.0, v29
	v_sub_f32_e32 v27, v27, v37
	v_add_f32_e32 v27, v28, v27
	v_add_f32_e32 v42, v29, v27
	v_rcp_f32_e32 v43, v42
	v_sub_f32_e32 v28, v29, v42
	v_add_f32_e32 v29, v31, v36
	v_add_f32_e32 v27, v27, v28
	v_sub_f32_e32 v28, v31, v29
	v_mul_f32_e32 v44, v29, v43
	v_add_f32_e32 v31, v36, v28
	v_mul_f32_e32 v36, v42, v44
	v_fma_f32 v38, v44, v42, -v36
	v_fmac_f32_e32 v38, v44, v27
	v_add_f32_e32 v28, v36, v38
	v_sub_f32_e32 v37, v29, v28
	v_pk_add_f32 v[40:41], v[28:29], v[36:37] neg_lo:[0,1] neg_hi:[0,1]
	v_mov_b32_e32 v39, v28
	v_pk_add_f32 v[28:29], v[40:41], v[38:39] neg_lo:[0,1] neg_hi:[0,1]
	v_cmp_neq_f32_e32 vcc, s13, v25
	v_add_f32_e32 v29, v31, v29
	v_add_f32_e32 v28, v28, v29
	v_add_f32_e32 v29, v37, v28
	v_mul_f32_e32 v31, v43, v29
	v_mul_f32_e32 v36, v42, v31
	v_fma_f32 v38, v31, v42, -v36
	v_fmac_f32_e32 v38, v31, v27
	v_sub_f32_e32 v27, v37, v29
	v_add_f32_e32 v27, v28, v27
	v_add_f32_e32 v28, v36, v38
	v_sub_f32_e32 v37, v29, v28
	v_pk_add_f32 v[40:41], v[28:29], v[36:37] neg_lo:[0,1] neg_hi:[0,1]
	v_mov_b32_e32 v39, v28
	v_pk_add_f32 v[28:29], v[40:41], v[38:39] neg_lo:[0,1] neg_hi:[0,1]
	v_cvt_f32_i32_e32 v36, v34
	v_add_f32_e32 v27, v27, v29
	v_add_f32_e32 v27, v28, v27
	v_add_f32_e32 v28, v44, v31
	v_add_f32_e32 v27, v37, v27
	v_sub_f32_e32 v29, v28, v44
	v_mul_f32_e32 v27, v43, v27
	v_sub_f32_e32 v29, v31, v29
	v_add_f32_e32 v27, v29, v27
	v_add_f32_e32 v31, v28, v27
	v_mul_f32_e32 v37, v31, v31
	v_fmamk_f32 v29, v37, 0x3e9b6dac, v55
	v_sub_f32_e32 v28, v31, v28
	v_fmaak_f32 v29, v37, v29, 0x3f2aaada
	v_sub_f32_e32 v27, v27, v28
	v_mul_f32_e32 v37, v31, v37
	v_mov_b32_e32 v28, 0x3f317218
	v_pk_mul_f32 v[40:41], v[36:37], v[28:29]
	v_ldexp_f32 v39, v31, 1
	v_fma_f32 v38, v36, s25, -v40
	v_fmac_f32_e32 v38, 0xb102e308, v36
	v_pk_add_f32 v[36:37], v[40:41], v[38:39]
	v_ldexp_f32 v27, v27, 1
	v_sub_f32_e32 v29, v37, v39
	v_sub_f32_e32 v29, v41, v29
	v_add_f32_e32 v43, v27, v29
	v_mov_b32_e32 v42, v40
	v_pk_add_f32 v[40:41], v[36:37], v[40:41] neg_lo:[0,1] neg_hi:[0,1]
	v_pk_add_f32 v[44:45], v[36:37], v[42:43]
	v_mov_b32_e32 v39, v36
	v_mov_b32_e32 v41, v45
	v_pk_add_f32 v[46:47], v[38:39], v[40:41] neg_lo:[0,1] neg_hi:[0,1]
	v_pk_add_f32 v[38:39], v[38:39], v[40:41]
	v_mov_b32_e32 v42, v43
	v_pk_add_f32 v[40:41], v[38:39], v[36:37] op_sel:[1,0] op_sel_hi:[0,1] neg_lo:[0,1] neg_hi:[0,1]
	v_pk_add_f32 v[48:49], v[44:45], v[40:41] op_sel_hi:[1,0] neg_lo:[0,1] neg_hi:[0,1]
	v_mov_b32_e32 v44, v45
	v_mov_b32_e32 v45, v39
	v_pk_mov_b32 v[40:41], v[36:37], v[40:41] op_sel:[1,0]
	v_mov_b32_e32 v43, v36
	v_pk_add_f32 v[40:41], v[44:45], v[40:41] neg_lo:[0,1] neg_hi:[0,1]
	v_mov_b32_e32 v48, v46
	v_pk_add_f32 v[36:37], v[42:43], v[40:41] neg_lo:[0,1] neg_hi:[0,1]
	v_mov_b32_e32 v47, v39
	v_pk_add_f32 v[40:41], v[48:49], v[36:37]
	s_mov_b32 s24, 0x3c23d70a
	v_pk_add_f32 v[42:43], v[40:41], v[40:41] op_sel:[0,1] op_sel_hi:[1,0]
	v_mov_b32_e32 v31, 0x41200000
	v_pk_add_f32 v[38:39], v[38:39], v[42:43] op_sel:[1,0] op_sel_hi:[0,1]
	v_mov_b32_e32 v41, v38
	v_pk_add_f32 v[44:45], v[40:41], v[46:47] neg_lo:[0,1] neg_hi:[0,1]
	v_mov_b32_e32 v37, v42
	v_sub_f32_e32 v27, v40, v44
	v_pk_add_f32 v[36:37], v[36:37], v[44:45] neg_lo:[0,1] neg_hi:[0,1]
	v_sub_f32_e32 v27, v46, v27
	v_add_f32_e32 v27, v36, v27
	v_add_f32_e32 v27, v27, v37
	v_add_f32_e32 v27, v38, v27
	v_cndmask_b32_e32 v27, v30, v27, vcc
	v_cmp_lt_f32_e64 vcc, |v25|, s15
	s_mov_b32 s14, 0xbd23d70a
	v_mov_b32_e32 v34, v26
	v_cndmask_b32_e32 v25, v27, v25, vcc
	v_add_f32_e32 v25, 0x358637bd, v25
	v_med3_f32 v25, v25, s24, v31
	v_div_scale_f32 v29, s[46:47], v25, v25, s14
	v_rcp_f32_e32 v36, v29
	s_waitcnt vmcnt(0)
	v_pk_mul_f32 v[26:27], v[32:33], v[34:35]
	v_mov_b32_e32 v49, 0x3f2aaada
	v_pk_mul_f32 v[26:27], v[26:27], s[6:7] op_sel_hi:[1,0]
	v_fma_f32 v32, -v29, v36, 1.0
	v_fmac_f32_e32 v36, v32, v36
	v_div_scale_f32 v32, vcc, s14, v25, s14
	v_mul_f32_e32 v33, v32, v36
	v_fma_f32 v34, -v29, v33, v32
	v_fmac_f32_e32 v33, v34, v36
	v_fma_f32 v29, -v29, v33, v32
	v_div_fmas_f32 v29, v29, v36, v33
	v_mul_f32_e32 v33, 0x3fb8aa3b, v50
	v_fma_f32 v34, v50, s3, -v33
	v_rndne_f32_e32 v35, v33
	v_fmac_f32_e32 v34, 0x32a5705f, v50
	v_sub_f32_e32 v33, v33, v35
	v_div_fixup_f32 v46, v29, v25, s14
	v_add_f32_e32 v33, v33, v34
	v_mul_f32_e32 v25, 0x3fb8aa3b, v46
	v_exp_f32_e32 v33, v33
	v_cvt_i32_f32_e32 v34, v35
	v_fma_f32 v29, v46, s3, -v25
	v_rndne_f32_e32 v32, v25
	v_fmac_f32_e32 v29, 0x32a5705f, v46
	v_sub_f32_e32 v25, v25, v32
	v_add_f32_e32 v25, v25, v29
	v_exp_f32_e32 v47, v25
	v_ldexp_f32 v25, v33, v34
	v_cmp_ngt_f32_e32 vcc, s7, v50
	v_cvt_i32_f32_e32 v48, v32
	v_cvt_pk_f16_f32 v17, v14, v15
	v_cndmask_b32_e32 v25, 0, v25, vcc
	v_cmp_nlt_f32_e32 vcc, s12, v50
	v_mov_b32_e32 v14, v4
	v_mov_b32_e32 v15, v4
	v_cndmask_b32_e32 v25, v30, v25, vcc
	v_add_f32_e32 v29, 1.0, v25
	v_add_f32_e32 v32, -1.0, v29
	v_sub_f32_e32 v33, v32, v29
	v_add_f32_e32 v33, 1.0, v33
	v_sub_f32_e32 v32, v25, v32
	v_add_f32_e32 v34, v32, v33
	v_frexp_mant_f32_e32 v35, v29
	v_cvt_f64_f32_e32 v[32:33], v29
	v_frexp_exp_i32_f64_e32 v32, v[32:33]
	v_cmp_gt_f32_e32 vcc, s33, v35
	v_cvt_pk_f16_f32 v18, v18, v19
	v_cvt_pk_f16_f32 v19, v20, v21
	v_subbrev_co_u32_e32 v40, vcc, 0, v32, vcc
	v_sub_u32_e32 v32, 0, v40
	v_ldexp_f32 v29, v29, v32
	v_ldexp_f32 v32, v34, v32
	v_add_f32_e32 v34, -1.0, v29
	v_add_f32_e32 v33, 1.0, v34
	v_sub_f32_e32 v33, v29, v33
	v_add_f32_e32 v35, v32, v33
	v_add_f32_e32 v33, 1.0, v29
	v_add_f32_e32 v36, -1.0, v33
	v_sub_f32_e32 v29, v29, v36
	v_add_f32_e32 v29, v32, v29
	v_add_f32_e32 v41, v33, v29
	v_rcp_f32_e32 v42, v41
	v_sub_f32_e32 v32, v33, v41
	v_add_f32_e32 v33, v34, v35
	v_add_f32_e32 v29, v29, v32
	v_mul_f32_e32 v44, v33, v42
	v_sub_f32_e32 v32, v34, v33
	v_mul_f32_e32 v34, v41, v44
	v_fma_f32 v36, v44, v41, -v34
	v_fmac_f32_e32 v36, v44, v29
	v_add_f32_e32 v43, v35, v32
	v_add_f32_e32 v32, v34, v36
	v_sub_f32_e32 v35, v33, v32
	v_pk_add_f32 v[38:39], v[32:33], v[34:35] neg_lo:[0,1] neg_hi:[0,1]
	v_mov_b32_e32 v37, v32
	v_pk_add_f32 v[32:33], v[38:39], v[36:37] neg_lo:[0,1] neg_hi:[0,1]
	v_cmp_neq_f32_e32 vcc, s13, v25
	v_add_f32_e32 v33, v43, v33
	v_add_f32_e32 v32, v32, v33
	v_add_f32_e32 v33, v35, v32
	v_mul_f32_e32 v43, v42, v33
	v_mul_f32_e32 v34, v41, v43
	v_fma_f32 v36, v43, v41, -v34
	v_fmac_f32_e32 v36, v43, v29
	v_sub_f32_e32 v29, v35, v33
	v_add_f32_e32 v29, v32, v29
	v_add_f32_e32 v32, v34, v36
	v_sub_f32_e32 v35, v33, v32
	v_pk_add_f32 v[38:39], v[32:33], v[34:35] neg_lo:[0,1] neg_hi:[0,1]
	v_mov_b32_e32 v37, v32
	v_pk_add_f32 v[32:33], v[38:39], v[36:37] neg_lo:[0,1] neg_hi:[0,1]
	v_mov_b32_e32 v20, v4
	v_add_f32_e32 v29, v29, v33
	v_add_f32_e32 v29, v32, v29
	v_add_f32_e32 v33, v44, v43
	v_add_f32_e32 v29, v35, v29
	v_sub_f32_e32 v32, v33, v44
	v_mul_f32_e32 v29, v42, v29
	v_sub_f32_e32 v32, v43, v32
	v_add_f32_e32 v34, v32, v29
	v_add_f32_e32 v36, v33, v34
	v_cvt_f32_i32_e32 v32, v40
	v_mul_f32_e32 v37, v36, v36
	v_sub_f32_e32 v33, v36, v33
	v_fmamk_f32 v29, v37, 0x3e9b6dac, v55
	v_sub_f32_e32 v33, v34, v33
	v_fmaak_f32 v29, v37, v29, 0x3f2aaada
	v_ldexp_f32 v38, v33, 1
	v_mul_f32_e32 v33, v36, v37
	v_ldexp_f32 v35, v36, 1
	v_pk_mul_f32 v[36:37], v[32:33], v[28:29]
	v_mov_b32_e32 v21, v4
	v_fma_f32 v34, v32, s25, -v36
	v_fmac_f32_e32 v34, 0xb102e308, v32
	v_pk_add_f32 v[32:33], v[36:37], v[34:35]
	s_nop 0
	v_sub_f32_e32 v29, v33, v35
	v_sub_f32_e32 v29, v37, v29
	v_add_f32_e32 v39, v38, v29
	v_mov_b32_e32 v38, v36
	v_pk_add_f32 v[36:37], v[32:33], v[36:37] neg_lo:[0,1] neg_hi:[0,1]
	v_pk_add_f32 v[40:41], v[32:33], v[38:39]
	v_mov_b32_e32 v35, v32
	v_mov_b32_e32 v37, v41
	v_pk_add_f32 v[42:43], v[34:35], v[36:37] neg_lo:[0,1] neg_hi:[0,1]
	v_pk_add_f32 v[34:35], v[34:35], v[36:37]
	v_mov_b32_e32 v38, v39
	v_pk_add_f32 v[36:37], v[34:35], v[32:33] op_sel:[1,0] op_sel_hi:[0,1] neg_lo:[0,1] neg_hi:[0,1]
	v_pk_add_f32 v[44:45], v[40:41], v[36:37] op_sel_hi:[1,0] neg_lo:[0,1] neg_hi:[0,1]
	v_mov_b32_e32 v40, v41
	v_mov_b32_e32 v41, v35
	v_pk_mov_b32 v[36:37], v[32:33], v[36:37] op_sel:[1,0]
	v_mov_b32_e32 v39, v32
	v_pk_add_f32 v[36:37], v[40:41], v[36:37] neg_lo:[0,1] neg_hi:[0,1]
	v_mov_b32_e32 v44, v42
	v_pk_add_f32 v[32:33], v[38:39], v[36:37] neg_lo:[0,1] neg_hi:[0,1]
	v_mov_b32_e32 v43, v35
	v_pk_add_f32 v[36:37], v[44:45], v[32:33]
	s_nop 0
	v_pk_add_f32 v[38:39], v[36:37], v[36:37] op_sel:[0,1] op_sel_hi:[1,0]
	s_nop 0
	v_pk_add_f32 v[34:35], v[34:35], v[38:39] op_sel:[1,0] op_sel_hi:[0,1]
	v_mov_b32_e32 v37, v34
	v_pk_add_f32 v[40:41], v[36:37], v[42:43] neg_lo:[0,1] neg_hi:[0,1]
	v_mov_b32_e32 v33, v38
	v_sub_f32_e32 v29, v36, v40
	v_pk_add_f32 v[32:33], v[32:33], v[40:41] neg_lo:[0,1] neg_hi:[0,1]
	v_sub_f32_e32 v29, v42, v29
	v_add_f32_e32 v29, v32, v29
	v_add_f32_e32 v29, v29, v33
	v_add_f32_e32 v29, v34, v29
	v_cndmask_b32_e32 v29, v30, v29, vcc
	v_cmp_lt_f32_e64 vcc, |v25|, s15
	s_nop 1
	v_cndmask_b32_e32 v25, v29, v25, vcc
	v_add_f32_e32 v25, 0x358637bd, v25
	v_med3_f32 v29, v25, s24, v31
	v_div_scale_f32 v32, s[46:47], v29, v29, s14
	v_rcp_f32_e32 v33, v32
	v_cvt_pk_f16_f32 v25, v26, v27
	v_ldexp_f32 v26, v47, v48
	v_fma_f32 v27, -v32, v33, 1.0
	v_fmac_f32_e32 v33, v27, v33
	v_div_scale_f32 v27, vcc, s14, v29, s14
	v_mul_f32_e32 v34, v27, v33
	v_fma_f32 v35, -v32, v34, v27
	v_fmac_f32_e32 v34, v35, v33
	v_fma_f32 v27, -v32, v34, v27
	v_div_fmas_f32 v27, v27, v33, v34
	v_div_fixup_f32 v27, v27, v29, s14
	v_mul_f32_e32 v29, 0x3fb8aa3b, v27
	v_fma_f32 v32, v27, s3, -v29
	v_rndne_f32_e32 v33, v29
	v_fmac_f32_e32 v32, 0x32a5705f, v27
	v_sub_f32_e32 v29, v29, v33
	v_add_f32_e32 v29, v29, v32
	v_exp_f32_e32 v29, v29
	v_cvt_i32_f32_e32 v32, v33
	v_cmp_ngt_f32_e32 vcc, s7, v46
	v_ldexp_f32 v29, v29, v32
	s_nop 0
	v_cndmask_b32_e32 v26, 0, v26, vcc
	v_cmp_nlt_f32_e32 vcc, s12, v46
	s_nop 1
	v_cndmask_b32_e32 v26, v30, v26, vcc
	v_cmp_ngt_f32_e32 vcc, s7, v27
	v_cndmask_b32_e64 v50, v26, 0, s[4:5]
	s_nop 0
	v_cndmask_b32_e32 v29, 0, v29, vcc
	v_cmp_nlt_f32_e32 vcc, s12, v27
	s_nop 1
	v_cndmask_b32_e32 v27, v30, v29, vcc
	v_mul_f32_e32 v29, 0x3fb8aa3b, v52
	v_fma_f32 v32, v52, s3, -v29
	v_rndne_f32_e32 v33, v29
	v_fmac_f32_e32 v32, 0x32a5705f, v52
	v_sub_f32_e32 v29, v29, v33
	v_add_f32_e32 v29, v29, v32
	v_exp_f32_e32 v29, v29
	v_cvt_i32_f32_e32 v32, v33
	v_cmp_ngt_f32_e32 vcc, s7, v52
	v_cndmask_b32_e64 v51, v27, 0, s[4:5]
	v_pk_add_f32 v[26:27], v[26:27], 1.0 op_sel_hi:[1,0] neg_lo:[1,0] neg_hi:[1,0]
	v_ldexp_f32 v29, v29, v32
	v_cndmask_b32_e32 v29, 0, v29, vcc
	v_cmp_nlt_f32_e32 vcc, s12, v52
	v_cndmask_b32_e64 v52, v26, 0, s[4:5]
	v_cndmask_b32_e64 v53, v27, 0, s[4:5]
	v_cndmask_b32_e32 v46, v30, v29, vcc
	v_add_f32_e32 v29, 1.0, v46
	v_add_f32_e32 v32, -1.0, v29
	v_sub_f32_e32 v33, v32, v29
	v_add_f32_e32 v33, 1.0, v33
	v_sub_f32_e32 v32, v46, v32
	v_add_f32_e32 v34, v32, v33
	v_frexp_mant_f32_e32 v35, v29
	v_cvt_f64_f32_e32 v[32:33], v29
	v_frexp_exp_i32_f64_e32 v32, v[32:33]
	v_cmp_gt_f32_e32 vcc, s33, v35
	s_nop 1
	v_subbrev_co_u32_e32 v40, vcc, 0, v32, vcc
	v_sub_u32_e32 v32, 0, v40
	v_ldexp_f32 v29, v29, v32
	v_ldexp_f32 v32, v34, v32
	v_add_f32_e32 v34, -1.0, v29
	v_add_f32_e32 v33, 1.0, v34
	v_sub_f32_e32 v33, v29, v33
	v_add_f32_e32 v35, v32, v33
	v_add_f32_e32 v33, 1.0, v29
	v_add_f32_e32 v36, -1.0, v33
	v_sub_f32_e32 v29, v29, v36
	v_add_f32_e32 v29, v32, v29
	v_add_f32_e32 v41, v33, v29
	v_rcp_f32_e32 v42, v41
	v_sub_f32_e32 v32, v33, v41
	v_add_f32_e32 v33, v34, v35
	v_add_f32_e32 v29, v29, v32
	v_mul_f32_e32 v44, v33, v42
	v_sub_f32_e32 v32, v34, v33
	v_mul_f32_e32 v34, v41, v44
	v_fma_f32 v36, v44, v41, -v34
	v_fmac_f32_e32 v36, v44, v29
	v_add_f32_e32 v43, v35, v32
	v_add_f32_e32 v32, v34, v36
	v_sub_f32_e32 v35, v33, v32
	v_pk_add_f32 v[38:39], v[32:33], v[34:35] neg_lo:[0,1] neg_hi:[0,1]
	v_mov_b32_e32 v37, v32
	v_pk_add_f32 v[32:33], v[38:39], v[36:37] neg_lo:[0,1] neg_hi:[0,1]
	v_cmp_neq_f32_e32 vcc, s13, v46
	v_add_f32_e32 v33, v43, v33
	v_add_f32_e32 v32, v32, v33
	v_add_f32_e32 v33, v35, v32
	v_mul_f32_e32 v43, v42, v33
	v_mul_f32_e32 v34, v41, v43
	v_fma_f32 v36, v43, v41, -v34
	v_fmac_f32_e32 v36, v43, v29
	v_sub_f32_e32 v29, v35, v33
	v_add_f32_e32 v29, v32, v29
	v_add_f32_e32 v32, v34, v36
	v_sub_f32_e32 v35, v33, v32
	v_pk_add_f32 v[38:39], v[32:33], v[34:35] neg_lo:[0,1] neg_hi:[0,1]
	v_mov_b32_e32 v37, v32
	v_pk_add_f32 v[32:33], v[38:39], v[36:37] neg_lo:[0,1] neg_hi:[0,1]
	s_nop 0
	v_add_f32_e32 v29, v29, v33
	v_add_f32_e32 v29, v32, v29
	v_add_f32_e32 v33, v44, v43
	v_add_f32_e32 v29, v35, v29
	v_sub_f32_e32 v32, v33, v44
	v_mul_f32_e32 v29, v42, v29
	v_sub_f32_e32 v32, v43, v32
	v_add_f32_e32 v34, v32, v29
	v_add_f32_e32 v36, v33, v34
	v_cvt_f32_i32_e32 v32, v40
	v_mul_f32_e32 v37, v36, v36
	v_sub_f32_e32 v33, v36, v33
	v_fmamk_f32 v29, v37, 0x3e9b6dac, v55
	v_sub_f32_e32 v33, v34, v33
	v_fmaak_f32 v29, v37, v29, 0x3f2aaada
	v_ldexp_f32 v38, v33, 1
	v_mul_f32_e32 v33, v36, v37
	v_ldexp_f32 v35, v36, 1
	v_pk_mul_f32 v[36:37], v[32:33], v[28:29]
	s_nop 0
	v_fma_f32 v34, v32, s25, -v36
	v_fmac_f32_e32 v34, 0xb102e308, v32
	v_pk_add_f32 v[32:33], v[36:37], v[34:35]
	s_nop 0
	v_sub_f32_e32 v29, v33, v35
	v_sub_f32_e32 v29, v37, v29
	v_add_f32_e32 v39, v38, v29
	v_mov_b32_e32 v38, v36
	v_pk_add_f32 v[36:37], v[32:33], v[36:37] neg_lo:[0,1] neg_hi:[0,1]
	v_pk_add_f32 v[40:41], v[32:33], v[38:39]
	v_mov_b32_e32 v35, v32
	v_mov_b32_e32 v37, v41
	v_pk_add_f32 v[42:43], v[34:35], v[36:37] neg_lo:[0,1] neg_hi:[0,1]
	v_pk_add_f32 v[34:35], v[34:35], v[36:37]
	v_mov_b32_e32 v38, v39
	v_pk_add_f32 v[36:37], v[34:35], v[32:33] op_sel:[1,0] op_sel_hi:[0,1] neg_lo:[0,1] neg_hi:[0,1]
	v_pk_add_f32 v[44:45], v[40:41], v[36:37] op_sel_hi:[1,0] neg_lo:[0,1] neg_hi:[0,1]
	v_mov_b32_e32 v40, v41
	v_mov_b32_e32 v41, v35
	v_pk_mov_b32 v[36:37], v[32:33], v[36:37] op_sel:[1,0]
	v_mov_b32_e32 v39, v32
	v_pk_add_f32 v[36:37], v[40:41], v[36:37] neg_lo:[0,1] neg_hi:[0,1]
	v_mov_b32_e32 v44, v42
	v_pk_add_f32 v[32:33], v[38:39], v[36:37] neg_lo:[0,1] neg_hi:[0,1]
	v_mov_b32_e32 v43, v35
	v_pk_add_f32 v[36:37], v[44:45], v[32:33]
	s_nop 0
	v_pk_add_f32 v[38:39], v[36:37], v[36:37] op_sel:[0,1] op_sel_hi:[1,0]
	s_nop 0
	v_pk_add_f32 v[34:35], v[34:35], v[38:39] op_sel:[1,0] op_sel_hi:[0,1]
	v_mov_b32_e32 v37, v34
	v_pk_add_f32 v[40:41], v[36:37], v[42:43] neg_lo:[0,1] neg_hi:[0,1]
	v_mov_b32_e32 v33, v38
	v_sub_f32_e32 v29, v36, v40
	v_pk_add_f32 v[32:33], v[32:33], v[40:41] neg_lo:[0,1] neg_hi:[0,1]
	v_sub_f32_e32 v29, v42, v29
	v_add_f32_e32 v29, v32, v29
	v_add_f32_e32 v29, v29, v33
	v_add_f32_e32 v29, v34, v29
	v_cndmask_b32_e32 v29, v30, v29, vcc
	v_cmp_lt_f32_e64 vcc, |v46|, s15
	v_pk_mul_f32 v[32:33], v[26:27], -2.0 op_sel_hi:[1,0]
	s_nop 0
	v_cndmask_b32_e32 v29, v29, v46, vcc
	v_add_f32_e32 v29, 0x358637bd, v29
	v_med3_f32 v29, v29, s24, v31
	v_div_scale_f32 v34, s[46:47], v29, v29, s14
	v_rcp_f32_e32 v35, v34
	s_nop 0
	v_fma_f32 v26, -v34, v35, 1.0
	v_fmac_f32_e32 v35, v26, v35
	v_div_scale_f32 v26, vcc, s14, v29, s14
	v_mul_f32_e32 v27, v26, v35
	v_fma_f32 v36, -v34, v27, v26
	v_fmac_f32_e32 v27, v36, v35
	v_fma_f32 v26, -v34, v27, v26
	v_mul_f32_e32 v34, 0x3fb8aa3b, v54
	v_div_fmas_f32 v26, v26, v35, v27
	v_fma_f32 v35, v54, s3, -v34
	v_rndne_f32_e32 v36, v34
	v_fmac_f32_e32 v35, 0x32a5705f, v54
	v_sub_f32_e32 v34, v34, v36
	v_div_fixup_f32 v44, v26, v29, s14
	v_add_f32_e32 v34, v34, v35
	v_mul_f32_e32 v26, 0x3fb8aa3b, v44
	v_exp_f32_e32 v34, v34
	v_cvt_i32_f32_e32 v35, v36
	v_fma_f32 v27, v44, s3, -v26
	v_rndne_f32_e32 v29, v26
	v_fmac_f32_e32 v27, 0x32a5705f, v44
	v_sub_f32_e32 v26, v26, v29
	v_add_f32_e32 v26, v26, v27
	v_exp_f32_e32 v45, v26
	v_ldexp_f32 v26, v34, v35
	v_cmp_ngt_f32_e32 vcc, s7, v54
	v_cvt_i32_f32_e32 v46, v29
	s_nop 0
	v_cndmask_b32_e32 v26, 0, v26, vcc
	v_cmp_nlt_f32_e32 vcc, s12, v54
	v_cndmask_b32_e64 v54, v32, 0, s[4:5]
	s_nop 0
	v_cndmask_b32_e32 v47, v30, v26, vcc
	v_add_f32_e32 v29, 1.0, v47
	v_add_f32_e32 v26, -1.0, v29
	v_sub_f32_e32 v27, v26, v29
	v_add_f32_e32 v27, 1.0, v27
	v_sub_f32_e32 v26, v47, v26
	v_add_f32_e32 v34, v26, v27
	v_frexp_mant_f32_e32 v35, v29
	v_cvt_f64_f32_e32 v[26:27], v29
	v_frexp_exp_i32_f64_e32 v26, v[26:27]
	v_cmp_gt_f32_e32 vcc, s33, v35
	s_nop 1
	v_subbrev_co_u32_e32 v40, vcc, 0, v26, vcc
	v_sub_u32_e32 v26, 0, v40
	v_ldexp_f32 v27, v29, v26
	v_add_f32_e32 v29, -1.0, v27
	v_add_f32_e32 v35, 1.0, v27
	v_ldexp_f32 v26, v34, v26
	v_add_f32_e32 v34, 1.0, v29
	v_add_f32_e32 v36, -1.0, v35
	v_sub_f32_e32 v34, v27, v34
	v_sub_f32_e32 v27, v27, v36
	v_add_f32_e32 v34, v26, v34
	v_add_f32_e32 v26, v26, v27
	v_add_f32_e32 v41, v35, v26
	v_rcp_f32_e32 v43, v41
	v_sub_f32_e32 v27, v35, v41
	v_add_f32_e32 v42, v26, v27
	v_add_f32_e32 v27, v29, v34
	v_sub_f32_e32 v26, v29, v27
	v_mul_f32_e32 v48, v27, v43
	v_add_f32_e32 v29, v34, v26
	v_mul_f32_e32 v34, v41, v48
	v_fma_f32 v36, v48, v41, -v34
	v_fmac_f32_e32 v36, v48, v42
	v_add_f32_e32 v26, v34, v36
	v_sub_f32_e32 v35, v27, v26
	v_pk_add_f32 v[38:39], v[26:27], v[34:35] neg_lo:[0,1] neg_hi:[0,1]
	v_mov_b32_e32 v37, v26
	v_pk_add_f32 v[26:27], v[38:39], v[36:37] neg_lo:[0,1] neg_hi:[0,1]
	v_cmp_neq_f32_e32 vcc, s13, v47
	v_add_f32_e32 v27, v29, v27
	v_add_f32_e32 v26, v26, v27
	v_add_f32_e32 v27, v35, v26
	v_mul_f32_e32 v29, v43, v27
	v_mul_f32_e32 v34, v41, v29
	v_fma_f32 v36, v29, v41, -v34
	v_fmac_f32_e32 v36, v29, v42
	v_sub_f32_e32 v35, v35, v27
	v_add_f32_e32 v41, v26, v35
	v_add_f32_e32 v26, v34, v36
	v_sub_f32_e32 v35, v27, v26
	v_pk_add_f32 v[38:39], v[26:27], v[34:35] neg_lo:[0,1] neg_hi:[0,1]
	v_mov_b32_e32 v37, v26
	v_pk_add_f32 v[26:27], v[38:39], v[36:37] neg_lo:[0,1] neg_hi:[0,1]
	s_nop 0
	v_add_f32_e32 v27, v41, v27
	v_add_f32_e32 v26, v26, v27
	v_add_f32_e32 v27, v48, v29
	v_add_f32_e32 v26, v35, v26
	v_sub_f32_e32 v34, v27, v48
	v_mul_f32_e32 v26, v43, v26
	v_sub_f32_e32 v29, v29, v34
	v_add_f32_e32 v29, v29, v26
	v_add_f32_e32 v34, v27, v29
	v_mul_f32_e32 v36, v34, v34
	v_cvt_f32_i32_e32 v26, v40
	v_fmac_f32_e32 v55, 0x3e9b6dac, v36
	v_sub_f32_e32 v27, v34, v27
	v_fmac_f32_e32 v49, v36, v55
	v_sub_f32_e32 v27, v29, v27
	v_ldexp_f32 v37, v27, 1
	v_mul_f32_e32 v27, v34, v36
	v_mov_b32_e32 v29, v49
	v_pk_mul_f32 v[28:29], v[26:27], v[28:29]
	v_ldexp_f32 v35, v34, 1
	v_fma_f32 v34, v26, s25, -v28
	v_fmac_f32_e32 v34, 0xb102e308, v26
	v_pk_add_f32 v[26:27], v[28:29], v[34:35]
	v_mov_b32_e32 v36, v28
	v_sub_f32_e32 v35, v27, v35
	v_sub_f32_e32 v35, v29, v35
	v_add_f32_e32 v37, v37, v35
	v_pk_add_f32 v[28:29], v[26:27], v[28:29] neg_lo:[0,1] neg_hi:[0,1]
	v_pk_add_f32 v[38:39], v[26:27], v[36:37]
	v_mov_b32_e32 v35, v26
	v_mov_b32_e32 v29, v39
	v_pk_add_f32 v[40:41], v[34:35], v[28:29] neg_lo:[0,1] neg_hi:[0,1]
	v_pk_add_f32 v[28:29], v[34:35], v[28:29]
	v_mov_b32_e32 v36, v37
	v_pk_add_f32 v[34:35], v[28:29], v[26:27] op_sel:[1,0] op_sel_hi:[0,1] neg_lo:[0,1] neg_hi:[0,1]
	v_pk_add_f32 v[42:43], v[38:39], v[34:35] op_sel_hi:[1,0] neg_lo:[0,1] neg_hi:[0,1]
	v_mov_b32_e32 v38, v39
	v_mov_b32_e32 v39, v29
	v_pk_mov_b32 v[34:35], v[26:27], v[34:35] op_sel:[1,0]
	v_mov_b32_e32 v37, v26
	v_pk_add_f32 v[34:35], v[38:39], v[34:35] neg_lo:[0,1] neg_hi:[0,1]
	v_mov_b32_e32 v42, v40
	v_pk_add_f32 v[26:27], v[36:37], v[34:35] neg_lo:[0,1] neg_hi:[0,1]
	v_mov_b32_e32 v41, v29
	v_pk_add_f32 v[34:35], v[42:43], v[26:27]
	v_cndmask_b32_e64 v55, v33, 0, s[4:5]
	v_pk_add_f32 v[36:37], v[34:35], v[34:35] op_sel:[0,1] op_sel_hi:[1,0]
	s_nop 0
	v_pk_add_f32 v[28:29], v[28:29], v[36:37] op_sel:[1,0] op_sel_hi:[0,1]
	v_mov_b32_e32 v35, v28
	v_pk_add_f32 v[38:39], v[34:35], v[40:41] neg_lo:[0,1] neg_hi:[0,1]
	v_mov_b32_e32 v27, v36
	v_sub_f32_e32 v29, v34, v38
	v_pk_add_f32 v[26:27], v[26:27], v[38:39] neg_lo:[0,1] neg_hi:[0,1]
	v_sub_f32_e32 v29, v40, v29
	v_add_f32_e32 v26, v26, v29
	v_add_f32_e32 v26, v26, v27
	v_add_f32_e32 v26, v28, v26
	v_cndmask_b32_e32 v26, v30, v26, vcc
	v_cmp_lt_f32_e64 vcc, |v47|, s15
	v_ldexp_f32 v29, v45, v46
	s_nop 0
	v_cndmask_b32_e32 v26, v26, v47, vcc
	v_add_f32_e32 v26, 0x358637bd, v26
	v_med3_f32 v26, v26, s24, v31
	v_div_scale_f32 v27, s[24:25], v26, v26, s14
	v_rcp_f32_e32 v28, v27
	s_nop 0
	v_fma_f32 v31, -v27, v28, 1.0
	v_fmac_f32_e32 v28, v31, v28
	v_div_scale_f32 v31, vcc, s14, v26, s14
	v_mul_f32_e32 v32, v31, v28
	v_fma_f32 v33, -v27, v32, v31
	v_fmac_f32_e32 v32, v33, v28
	v_fma_f32 v27, -v27, v32, v31
	v_div_fmas_f32 v27, v27, v28, v32
	v_div_fixup_f32 v27, v27, v26, s14
	v_mul_f32_e32 v26, 0x3fb8aa3b, v27
	v_fma_f32 v28, v27, s3, -v26
	v_rndne_f32_e32 v31, v26
	v_fmac_f32_e32 v28, 0x32a5705f, v27
	v_sub_f32_e32 v26, v26, v31
	v_add_f32_e32 v26, v26, v28
	v_exp_f32_e32 v28, v26
	v_cvt_i32_f32_e32 v31, v31
	v_cmp_ngt_f32_e32 vcc, s7, v44
	s_movk_i32 s3, 0xc0
	v_mov_b32_e32 v32, v4
	v_cndmask_b32_e32 v26, 0, v29, vcc
	v_cmp_nlt_f32_e32 vcc, s12, v44
	v_ldexp_f32 v28, v28, v31
	v_mov_b32_e32 v31, v4
	v_cndmask_b32_e32 v26, v30, v26, vcc
	v_cmp_ngt_f32_e32 vcc, s7, v27
	v_cndmask_b32_e64 v56, v26, 0, s[4:5]
	v_cmp_eq_u32_e64 s[6:7], 0, v64
	v_cndmask_b32_e32 v28, 0, v28, vcc
	v_cmp_nlt_f32_e32 vcc, s12, v27
	v_mov_b32_e32 v33, v4
	s_nop 0
	v_cndmask_b32_e32 v27, v30, v28, vcc
	v_cndmask_b32_e64 v57, v27, 0, s[4:5]
	v_pk_add_f32 v[26:27], v[26:27], 1.0 op_sel_hi:[1,0] neg_lo:[1,0] neg_hi:[1,0]
	v_mov_b32_e32 v30, v4
	v_pk_mul_f32 v[28:29], v[26:27], -2.0 op_sel_hi:[1,0]
	v_cndmask_b32_e64 v59, v27, 0, s[4:5]
	v_cndmask_b32_e64 v60, v28, 0, s[4:5]
	v_lshlrev_b32_e32 v27, 6, v64
	v_mov_b32_e32 v28, 0x80
	v_cndmask_b32_e64 v27, v27, v28, s[4:5]
	v_mad_u32_u24 v27, v65, s3, v27
	v_cndmask_b32_e64 v58, v26, 0, s[4:5]
	v_mul_u32_u24_e32 v26, 0xc0, v65
	v_and_or_b32 v62, v0, 48, v27
	v_lshlrev_b32_e32 v27, 6, v65
	v_sub_u32_e32 v26, v26, v27
	v_lshl_add_u32 v26, v1, 5, v26
	v_cndmask_b32_e64 v61, v29, 0, s[4:5]
	v_lshl_or_b32 v63, v64, 3, v26
	v_cmp_gt_u32_e64 s[4:5], 2, v64
	s_mov_b32 s3, -2
	v_mov_b32_e32 v166, v6
	v_mov_b32_e32 v167, v7
	v_mov_b32_e32 v168, v8
	v_mov_b32_e32 v169, v9
	v_mov_b32_e32 v170, v2
	v_mov_b32_e32 v171, v3
	v_mov_b32_e32 v172, v4
	v_mov_b32_e32 v173, v5
	v_mov_b32_e32 v6, v166
	v_mov_b32_e32 v7, v168
	v_mov_b32_e32 v8, v170
	v_mov_b32_e32 v9, v172
	v_mov_b32_e32 v2, v167
	v_mov_b32_e32 v3, v169
	v_mov_b32_e32 v4, v171
	v_mov_b32_e32 v5, v173
	v_mov_b32_e32 v166, v10
	v_mov_b32_e32 v167, v11
	v_mov_b32_e32 v168, v12
	v_mov_b32_e32 v169, v13
	v_mov_b32_e32 v170, v14
	v_mov_b32_e32 v171, v15
	v_mov_b32_e32 v172, v16
	v_mov_b32_e32 v173, v17
	v_mov_b32_e32 v10, v166
	v_mov_b32_e32 v11, v168
	v_mov_b32_e32 v12, v170
	v_mov_b32_e32 v13, v172
	v_mov_b32_e32 v14, v167
	v_mov_b32_e32 v15, v169
	v_mov_b32_e32 v16, v171
	v_mov_b32_e32 v17, v173
	v_mov_b32_e32 v166, v18
	v_mov_b32_e32 v167, v19
	v_mov_b32_e32 v168, v20
	v_mov_b32_e32 v169, v21
	v_mov_b32_e32 v170, v22
	v_mov_b32_e32 v171, v23
	v_mov_b32_e32 v172, v24
	v_mov_b32_e32 v173, v25
	v_mov_b32_e32 v18, v166
	v_mov_b32_e32 v19, v168
	v_mov_b32_e32 v20, v170
	v_mov_b32_e32 v21, v172
	v_mov_b32_e32 v22, v167
	v_mov_b32_e32 v23, v169
	v_mov_b32_e32 v24, v171
	v_mov_b32_e32 v25, v173
	v_mov_b32_e32 v124, 0
	v_mov_b32_e32 v125, 0
	v_mov_b32_e32 v126, 0
	v_mov_b32_e32 v127, 0
	v_mov_b32_e32 v128, 0
	v_mov_b32_e32 v129, 0
	v_mov_b32_e32 v130, 0
	v_mov_b32_e32 v131, 0
	v_mov_b32_e32 v148, 0
	v_mov_b32_e32 v149, 0
	v_mov_b32_e32 v150, 0
	v_mov_b32_e32 v151, 0
	v_mov_b32_e32 v168, 0
	v_mov_b32_e32 v169, 0
	v_mov_b32_e32 v170, 0
	v_mov_b32_e32 v171, 0
	v_mov_b32_e32 v152, v52
	v_mov_b32_e32 v153, v53
	v_mov_b32_e32 v154, v58
	v_mov_b32_e32 v155, v59
	s_waitcnt lgkmcnt(0)
	s_barrier
	s_waitcnt lgkmcnt(0)
	s_barrier
	s_mov_b32 s3, 0
	v_mfma_f32_16x16x32_f16 v[132:135], v[6:9], v[124:127], v[168:171]
	v_mfma_f32_16x16x32_f16 v[136:139], v[10:13], v[124:127], v[168:171]
	v_mfma_f32_16x16x32_f16 v[140:143], v[18:21], v[124:127], v[168:171]
	s_nop 0
	v_mfma_f32_16x16x32_f16 v[132:135], v[2:5], v[128:131], v[132:135]
	s_nop 1
	v_mfma_f32_16x16x32_f16 v[136:139], v[14:17], v[128:131], v[136:139]
	s_nop 1
	v_mfma_f32_16x16x32_f16 v[140:143], v[22:25], v[128:131], v[140:143]
	s_branch .LBB3_49

.LBB3_49:
	s_and_b32 s12, s3, 1
	s_mul_i32 s13, s12, 0x3100
	s_mulk_i32 s12, 0x2100
	v_add_u32_e32 v165, s13, v62
	v_add_u32_e32 v164, s12, v63
	s_nop 0
	ds_read_b128 v[64:67], v165 offset:33792
	ds_read_b128 v[68:71], v165 offset:34576
	ds_read_b128 v[72:75], v165 offset:35360
	ds_read_b128 v[76:79], v165 offset:36144
	ds_read_b128 v[80:83], v165 offset:36928
	ds_read_b128 v[84:87], v165 offset:37712
	ds_read_b128 v[88:91], v165 offset:38496
	ds_read_b128 v[92:95], v165 offset:39280
	ds_read_b128 v[96:99], v165 offset:40064
	ds_read_b128 v[100:103], v165 offset:40848
	ds_read_b128 v[104:107], v165 offset:41632
	ds_read_b128 v[108:111], v165 offset:42416
	ds_read_b128 v[112:115], v165 offset:43200
	ds_read_b128 v[116:119], v165 offset:43984
	ds_read_b128 v[120:123], v165 offset:44768
	ds_read_b128 v[44:47], v165 offset:45552
	s_waitcnt lgkmcnt(15)
	s_nop 2
	v_cndmask_b32_e64 v160, v136, v132, s[6:7]
	v_cndmask_b32_e64 v161, v137, v133, s[6:7]
	v_cndmask_b32_e64 v162, v138, v134, s[6:7]
	v_cndmask_b32_e64 v163, v139, v135, s[6:7]
	v_cndmask_b32_e64 v156, v140, v160, s[4:5]
	v_cndmask_b32_e64 v157, v141, v161, s[4:5]
	v_add_f32_e32 v156, v156, v64
	v_add_f32_e32 v157, v157, v65
	v_exp_f32_e32 v156, v156
	v_exp_f32_e32 v157, v157
	v_cndmask_b32_e64 v158, v142, v162, s[4:5]
	v_cndmask_b32_e64 v159, v143, v163, s[4:5]
	v_add_f32_e32 v158, v158, v66
	v_add_f32_e32 v159, v159, v67
	v_pk_add_f32 v[156:157], v[156:157], 1.0 op_sel_hi:[1,0]
	v_exp_f32_e32 v158, v158
	v_rcp_f32_e32 v156, v156
	v_rcp_f32_e32 v157, v157
	v_exp_f32_e32 v159, v159
	v_pk_fma_f32 v[148:149], v[54:55], v[156:157], v[152:153]
	v_pk_add_f32 v[158:159], v[158:159], 1.0 op_sel_hi:[1,0]
	v_cvt_pk_f16_f32 v124, v148, v149
	v_rcp_f32_e32 v158, v158
	v_rcp_f32_e32 v159, v159
	v_mov_b32_dpp v125, v124 quad_perm:[1,2,3,0] row_mask:0xf bank_mask:0xf bound_ctrl:1
	v_mov_b32_dpp v126, v124 quad_perm:[2,3,0,1] row_mask:0xf bank_mask:0xf bound_ctrl:1
	v_mov_b32_dpp v127, v124 quad_perm:[3,0,1,2] row_mask:0xf bank_mask:0xf bound_ctrl:1
	v_pk_fma_f32 v[150:151], v[60:61], v[158:159], v[154:155]
	s_waitcnt lgkmcnt(14)
	v_mfma_f32_16x16x32_f16 v[132:135], v[6:9], v[124:127], v[68:71]
	v_cvt_pk_f16_f32 v128, v150, v151
	s_nop 0
	v_mfma_f32_16x16x32_f16 v[136:139], v[10:13], v[124:127], v[68:71]
	v_mov_b32_dpp v129, v128 quad_perm:[1,2,3,0] row_mask:0xf bank_mask:0xf bound_ctrl:1
	v_mov_b32_dpp v130, v128 quad_perm:[2,3,0,1] row_mask:0xf bank_mask:0xf bound_ctrl:1
	v_mfma_f32_16x16x32_f16 v[140:143], v[18:21], v[124:127], v[68:71]
	v_mov_b32_dpp v131, v128 quad_perm:[3,0,1,2] row_mask:0xf bank_mask:0xf bound_ctrl:1
	s_nop 1
	v_mfma_f32_16x16x32_f16 v[132:135], v[2:5], v[128:131], v[132:135]
	v_fma_f32 v154, v56, v150, v58
	v_fma_f32 v155, v57, v151, v59
	v_mfma_f32_16x16x32_f16 v[136:139], v[14:17], v[128:131], v[136:139]
	v_fma_f32 v152, v50, v148, v52
	v_fma_f32 v153, v51, v149, v53
	v_mfma_f32_16x16x32_f16 v[140:143], v[22:25], v[128:131], v[140:143]
	ds_write_b32 v164, v124 offset:16896
	ds_write_b32 v164, v128 offset:16900
	s_nop 2
	v_cndmask_b32_e64 v160, v136, v132, s[6:7]
	v_cndmask_b32_e64 v161, v137, v133, s[6:7]
	v_cndmask_b32_e64 v162, v138, v134, s[6:7]
	v_cndmask_b32_e64 v163, v139, v135, s[6:7]
	v_cndmask_b32_e64 v156, v140, v160, s[4:5]
	v_cndmask_b32_e64 v157, v141, v161, s[4:5]
	v_exp_f32_e32 v156, v156
	v_exp_f32_e32 v157, v157
	v_cndmask_b32_e64 v158, v142, v162, s[4:5]
	v_cndmask_b32_e64 v159, v143, v163, s[4:5]
	v_pk_add_f32 v[156:157], v[156:157], 1.0 op_sel_hi:[1,0]
	v_exp_f32_e32 v158, v158
	v_rcp_f32_e32 v156, v156
	v_rcp_f32_e32 v157, v157
	v_exp_f32_e32 v159, v159
	v_pk_fma_f32 v[148:149], v[54:55], v[156:157], v[152:153]
	v_pk_add_f32 v[158:159], v[158:159], 1.0 op_sel_hi:[1,0]
	v_cvt_pk_f16_f32 v124, v148, v149
	v_rcp_f32_e32 v158, v158
	v_rcp_f32_e32 v159, v159
	v_mov_b32_dpp v125, v124 quad_perm:[1,2,3,0] row_mask:0xf bank_mask:0xf bound_ctrl:1
	v_mov_b32_dpp v126, v124 quad_perm:[2,3,0,1] row_mask:0xf bank_mask:0xf bound_ctrl:1
	v_mov_b32_dpp v127, v124 quad_perm:[3,0,1,2] row_mask:0xf bank_mask:0xf bound_ctrl:1
	v_pk_fma_f32 v[150:151], v[60:61], v[158:159], v[154:155]
	s_waitcnt lgkmcnt(15)
	v_mfma_f32_16x16x32_f16 v[132:135], v[6:9], v[124:127], v[72:75]
	v_cvt_pk_f16_f32 v128, v150, v151
	s_nop 0
	v_mfma_f32_16x16x32_f16 v[136:139], v[10:13], v[124:127], v[72:75]
	v_mov_b32_dpp v129, v128 quad_perm:[1,2,3,0] row_mask:0xf bank_mask:0xf bound_ctrl:1
	v_mov_b32_dpp v130, v128 quad_perm:[2,3,0,1] row_mask:0xf bank_mask:0xf bound_ctrl:1
	v_mfma_f32_16x16x32_f16 v[140:143], v[18:21], v[124:127], v[72:75]
	v_mov_b32_dpp v131, v128 quad_perm:[3,0,1,2] row_mask:0xf bank_mask:0xf bound_ctrl:1
	s_nop 1
	v_mfma_f32_16x16x32_f16 v[132:135], v[2:5], v[128:131], v[132:135]
	v_fma_f32 v154, v56, v150, v58
	v_fma_f32 v155, v57, v151, v59
	v_mfma_f32_16x16x32_f16 v[136:139], v[14:17], v[128:131], v[136:139]
	v_fma_f32 v152, v50, v148, v52
	v_fma_f32 v153, v51, v149, v53
	v_mfma_f32_16x16x32_f16 v[140:143], v[22:25], v[128:131], v[140:143]
	ds_write_b32 v164, v124 offset:17424
	ds_write_b32 v164, v128 offset:17428
	s_nop 2
	v_cndmask_b32_e64 v160, v136, v132, s[6:7]
	v_cndmask_b32_e64 v161, v137, v133, s[6:7]
	v_cndmask_b32_e64 v162, v138, v134, s[6:7]
	v_cndmask_b32_e64 v163, v139, v135, s[6:7]
	v_cndmask_b32_e64 v156, v140, v160, s[4:5]
	v_cndmask_b32_e64 v157, v141, v161, s[4:5]
	v_exp_f32_e32 v156, v156
	v_exp_f32_e32 v157, v157
	v_cndmask_b32_e64 v158, v142, v162, s[4:5]
	v_cndmask_b32_e64 v159, v143, v163, s[4:5]
	v_pk_add_f32 v[156:157], v[156:157], 1.0 op_sel_hi:[1,0]
	v_exp_f32_e32 v158, v158
	v_rcp_f32_e32 v156, v156
	v_rcp_f32_e32 v157, v157
	v_exp_f32_e32 v159, v159
	v_pk_fma_f32 v[148:149], v[54:55], v[156:157], v[152:153]
	v_pk_add_f32 v[158:159], v[158:159], 1.0 op_sel_hi:[1,0]
	v_cvt_pk_f16_f32 v124, v148, v149
	v_rcp_f32_e32 v158, v158
	v_rcp_f32_e32 v159, v159
	v_mov_b32_dpp v125, v124 quad_perm:[1,2,3,0] row_mask:0xf bank_mask:0xf bound_ctrl:1
	v_mov_b32_dpp v126, v124 quad_perm:[2,3,0,1] row_mask:0xf bank_mask:0xf bound_ctrl:1
	v_mov_b32_dpp v127, v124 quad_perm:[3,0,1,2] row_mask:0xf bank_mask:0xf bound_ctrl:1
	v_pk_fma_f32 v[150:151], v[60:61], v[158:159], v[154:155]
	s_waitcnt lgkmcnt(15)
	v_mfma_f32_16x16x32_f16 v[132:135], v[6:9], v[124:127], v[76:79]
	v_cvt_pk_f16_f32 v128, v150, v151
	s_nop 0
	v_mfma_f32_16x16x32_f16 v[136:139], v[10:13], v[124:127], v[76:79]
	v_mov_b32_dpp v129, v128 quad_perm:[1,2,3,0] row_mask:0xf bank_mask:0xf bound_ctrl:1
	v_mov_b32_dpp v130, v128 quad_perm:[2,3,0,1] row_mask:0xf bank_mask:0xf bound_ctrl:1
	v_mfma_f32_16x16x32_f16 v[140:143], v[18:21], v[124:127], v[76:79]
	v_mov_b32_dpp v131, v128 quad_perm:[3,0,1,2] row_mask:0xf bank_mask:0xf bound_ctrl:1
	s_nop 1
	v_mfma_f32_16x16x32_f16 v[132:135], v[2:5], v[128:131], v[132:135]
	v_fma_f32 v154, v56, v150, v58
	v_fma_f32 v155, v57, v151, v59
	v_mfma_f32_16x16x32_f16 v[136:139], v[14:17], v[128:131], v[136:139]
	v_fma_f32 v152, v50, v148, v52
	v_fma_f32 v153, v51, v149, v53
	v_mfma_f32_16x16x32_f16 v[140:143], v[22:25], v[128:131], v[140:143]
	ds_write_b32 v164, v124 offset:17952
	ds_write_b32 v164, v128 offset:17956
	s_nop 2
	v_cndmask_b32_e64 v160, v136, v132, s[6:7]
	v_cndmask_b32_e64 v161, v137, v133, s[6:7]
	v_cndmask_b32_e64 v162, v138, v134, s[6:7]
	v_cndmask_b32_e64 v163, v139, v135, s[6:7]
	v_cndmask_b32_e64 v156, v140, v160, s[4:5]
	v_cndmask_b32_e64 v157, v141, v161, s[4:5]
	v_exp_f32_e32 v156, v156
	v_exp_f32_e32 v157, v157
	v_cndmask_b32_e64 v158, v142, v162, s[4:5]
	v_cndmask_b32_e64 v159, v143, v163, s[4:5]
	v_pk_add_f32 v[156:157], v[156:157], 1.0 op_sel_hi:[1,0]
	v_exp_f32_e32 v158, v158
	v_rcp_f32_e32 v156, v156
	v_rcp_f32_e32 v157, v157
	v_exp_f32_e32 v159, v159
	v_pk_fma_f32 v[148:149], v[54:55], v[156:157], v[152:153]
	v_pk_add_f32 v[158:159], v[158:159], 1.0 op_sel_hi:[1,0]
	v_cvt_pk_f16_f32 v124, v148, v149
	v_rcp_f32_e32 v158, v158
	v_rcp_f32_e32 v159, v159
	v_mov_b32_dpp v125, v124 quad_perm:[1,2,3,0] row_mask:0xf bank_mask:0xf bound_ctrl:1
	v_mov_b32_dpp v126, v124 quad_perm:[2,3,0,1] row_mask:0xf bank_mask:0xf bound_ctrl:1
	v_mov_b32_dpp v127, v124 quad_perm:[3,0,1,2] row_mask:0xf bank_mask:0xf bound_ctrl:1
	v_pk_fma_f32 v[150:151], v[60:61], v[158:159], v[154:155]
	s_waitcnt lgkmcnt(15)
	v_mfma_f32_16x16x32_f16 v[132:135], v[6:9], v[124:127], v[80:83]
	v_cvt_pk_f16_f32 v128, v150, v151
	s_nop 0
	v_mfma_f32_16x16x32_f16 v[136:139], v[10:13], v[124:127], v[80:83]
	v_mov_b32_dpp v129, v128 quad_perm:[1,2,3,0] row_mask:0xf bank_mask:0xf bound_ctrl:1
	v_mov_b32_dpp v130, v128 quad_perm:[2,3,0,1] row_mask:0xf bank_mask:0xf bound_ctrl:1
	v_mfma_f32_16x16x32_f16 v[140:143], v[18:21], v[124:127], v[80:83]
	v_mov_b32_dpp v131, v128 quad_perm:[3,0,1,2] row_mask:0xf bank_mask:0xf bound_ctrl:1
	s_nop 1
	v_mfma_f32_16x16x32_f16 v[132:135], v[2:5], v[128:131], v[132:135]
	v_fma_f32 v154, v56, v150, v58
	v_fma_f32 v155, v57, v151, v59
	v_mfma_f32_16x16x32_f16 v[136:139], v[14:17], v[128:131], v[136:139]
	v_fma_f32 v152, v50, v148, v52
	v_fma_f32 v153, v51, v149, v53
	v_mfma_f32_16x16x32_f16 v[140:143], v[22:25], v[128:131], v[140:143]
	ds_write_b32 v164, v124 offset:18480
	ds_write_b32 v164, v128 offset:18484
	s_nop 2
	v_cndmask_b32_e64 v160, v136, v132, s[6:7]
	v_cndmask_b32_e64 v161, v137, v133, s[6:7]
	v_cndmask_b32_e64 v162, v138, v134, s[6:7]
	v_cndmask_b32_e64 v163, v139, v135, s[6:7]
	v_cndmask_b32_e64 v156, v140, v160, s[4:5]
	v_cndmask_b32_e64 v157, v141, v161, s[4:5]
	v_exp_f32_e32 v156, v156
	v_exp_f32_e32 v157, v157
	v_cndmask_b32_e64 v158, v142, v162, s[4:5]
	v_cndmask_b32_e64 v159, v143, v163, s[4:5]
	v_pk_add_f32 v[156:157], v[156:157], 1.0 op_sel_hi:[1,0]
	v_exp_f32_e32 v158, v158
	v_rcp_f32_e32 v156, v156
	v_rcp_f32_e32 v157, v157
	v_exp_f32_e32 v159, v159
	v_pk_fma_f32 v[148:149], v[54:55], v[156:157], v[152:153]
	v_pk_add_f32 v[158:159], v[158:159], 1.0 op_sel_hi:[1,0]
	v_cvt_pk_f16_f32 v124, v148, v149
	v_rcp_f32_e32 v158, v158
	v_rcp_f32_e32 v159, v159
	v_mov_b32_dpp v125, v124 quad_perm:[1,2,3,0] row_mask:0xf bank_mask:0xf bound_ctrl:1
	v_mov_b32_dpp v126, v124 quad_perm:[2,3,0,1] row_mask:0xf bank_mask:0xf bound_ctrl:1
	v_mov_b32_dpp v127, v124 quad_perm:[3,0,1,2] row_mask:0xf bank_mask:0xf bound_ctrl:1
	v_pk_fma_f32 v[150:151], v[60:61], v[158:159], v[154:155]
	s_waitcnt lgkmcnt(15)
	v_mfma_f32_16x16x32_f16 v[132:135], v[6:9], v[124:127], v[84:87]
	v_cvt_pk_f16_f32 v128, v150, v151
	s_nop 0
	v_mfma_f32_16x16x32_f16 v[136:139], v[10:13], v[124:127], v[84:87]
	v_mov_b32_dpp v129, v128 quad_perm:[1,2,3,0] row_mask:0xf bank_mask:0xf bound_ctrl:1
	v_mov_b32_dpp v130, v128 quad_perm:[2,3,0,1] row_mask:0xf bank_mask:0xf bound_ctrl:1
	v_mfma_f32_16x16x32_f16 v[140:143], v[18:21], v[124:127], v[84:87]
	v_mov_b32_dpp v131, v128 quad_perm:[3,0,1,2] row_mask:0xf bank_mask:0xf bound_ctrl:1
	s_nop 1
	v_mfma_f32_16x16x32_f16 v[132:135], v[2:5], v[128:131], v[132:135]
	v_fma_f32 v154, v56, v150, v58
	v_fma_f32 v155, v57, v151, v59
	v_mfma_f32_16x16x32_f16 v[136:139], v[14:17], v[128:131], v[136:139]
	v_fma_f32 v152, v50, v148, v52
	v_fma_f32 v153, v51, v149, v53
	v_mfma_f32_16x16x32_f16 v[140:143], v[22:25], v[128:131], v[140:143]
	ds_write_b32 v164, v124 offset:19008
	ds_write_b32 v164, v128 offset:19012
	s_nop 2
	v_cndmask_b32_e64 v160, v136, v132, s[6:7]
	v_cndmask_b32_e64 v161, v137, v133, s[6:7]
	v_cndmask_b32_e64 v162, v138, v134, s[6:7]
	v_cndmask_b32_e64 v163, v139, v135, s[6:7]
	v_cndmask_b32_e64 v156, v140, v160, s[4:5]
	v_cndmask_b32_e64 v157, v141, v161, s[4:5]
	v_exp_f32_e32 v156, v156
	v_exp_f32_e32 v157, v157
	v_cndmask_b32_e64 v158, v142, v162, s[4:5]
	v_cndmask_b32_e64 v159, v143, v163, s[4:5]
	v_pk_add_f32 v[156:157], v[156:157], 1.0 op_sel_hi:[1,0]
	v_exp_f32_e32 v158, v158
	v_rcp_f32_e32 v156, v156
	v_rcp_f32_e32 v157, v157
	v_exp_f32_e32 v159, v159
	v_pk_fma_f32 v[148:149], v[54:55], v[156:157], v[152:153]
	v_pk_add_f32 v[158:159], v[158:159], 1.0 op_sel_hi:[1,0]
	v_cvt_pk_f16_f32 v124, v148, v149
	v_rcp_f32_e32 v158, v158
	v_rcp_f32_e32 v159, v159
	v_mov_b32_dpp v125, v124 quad_perm:[1,2,3,0] row_mask:0xf bank_mask:0xf bound_ctrl:1
	v_mov_b32_dpp v126, v124 quad_perm:[2,3,0,1] row_mask:0xf bank_mask:0xf bound_ctrl:1
	v_mov_b32_dpp v127, v124 quad_perm:[3,0,1,2] row_mask:0xf bank_mask:0xf bound_ctrl:1
	v_pk_fma_f32 v[150:151], v[60:61], v[158:159], v[154:155]
	s_waitcnt lgkmcnt(15)
	v_mfma_f32_16x16x32_f16 v[132:135], v[6:9], v[124:127], v[88:91]
	v_cvt_pk_f16_f32 v128, v150, v151
	s_nop 0
	v_mfma_f32_16x16x32_f16 v[136:139], v[10:13], v[124:127], v[88:91]
	v_mov_b32_dpp v129, v128 quad_perm:[1,2,3,0] row_mask:0xf bank_mask:0xf bound_ctrl:1
	v_mov_b32_dpp v130, v128 quad_perm:[2,3,0,1] row_mask:0xf bank_mask:0xf bound_ctrl:1
	v_mfma_f32_16x16x32_f16 v[140:143], v[18:21], v[124:127], v[88:91]
	v_mov_b32_dpp v131, v128 quad_perm:[3,0,1,2] row_mask:0xf bank_mask:0xf bound_ctrl:1
	s_nop 1
	v_mfma_f32_16x16x32_f16 v[132:135], v[2:5], v[128:131], v[132:135]
	v_fma_f32 v154, v56, v150, v58
	v_fma_f32 v155, v57, v151, v59
	v_mfma_f32_16x16x32_f16 v[136:139], v[14:17], v[128:131], v[136:139]
	v_fma_f32 v152, v50, v148, v52
	v_fma_f32 v153, v51, v149, v53
	v_mfma_f32_16x16x32_f16 v[140:143], v[22:25], v[128:131], v[140:143]
	ds_write_b32 v164, v124 offset:19536
	ds_write_b32 v164, v128 offset:19540
	s_nop 2
	v_cndmask_b32_e64 v160, v136, v132, s[6:7]
	v_cndmask_b32_e64 v161, v137, v133, s[6:7]
	v_cndmask_b32_e64 v162, v138, v134, s[6:7]
	v_cndmask_b32_e64 v163, v139, v135, s[6:7]
	v_cndmask_b32_e64 v156, v140, v160, s[4:5]
	v_cndmask_b32_e64 v157, v141, v161, s[4:5]
	v_exp_f32_e32 v156, v156
	v_exp_f32_e32 v157, v157
	v_cndmask_b32_e64 v158, v142, v162, s[4:5]
	v_cndmask_b32_e64 v159, v143, v163, s[4:5]
	v_pk_add_f32 v[156:157], v[156:157], 1.0 op_sel_hi:[1,0]
	v_exp_f32_e32 v158, v158
	v_rcp_f32_e32 v156, v156
	v_rcp_f32_e32 v157, v157
	v_exp_f32_e32 v159, v159
	v_pk_fma_f32 v[148:149], v[54:55], v[156:157], v[152:153]
	v_pk_add_f32 v[158:159], v[158:159], 1.0 op_sel_hi:[1,0]
	v_cvt_pk_f16_f32 v124, v148, v149
	v_rcp_f32_e32 v158, v158
	v_rcp_f32_e32 v159, v159
	v_mov_b32_dpp v125, v124 quad_perm:[1,2,3,0] row_mask:0xf bank_mask:0xf bound_ctrl:1
	v_mov_b32_dpp v126, v124 quad_perm:[2,3,0,1] row_mask:0xf bank_mask:0xf bound_ctrl:1
	v_mov_b32_dpp v127, v124 quad_perm:[3,0,1,2] row_mask:0xf bank_mask:0xf bound_ctrl:1
	v_pk_fma_f32 v[150:151], v[60:61], v[158:159], v[154:155]
	s_waitcnt lgkmcnt(15)
	v_mfma_f32_16x16x32_f16 v[132:135], v[6:9], v[124:127], v[92:95]
	v_cvt_pk_f16_f32 v128, v150, v151
	s_nop 0
	v_mfma_f32_16x16x32_f16 v[136:139], v[10:13], v[124:127], v[92:95]
	v_mov_b32_dpp v129, v128 quad_perm:[1,2,3,0] row_mask:0xf bank_mask:0xf bound_ctrl:1
	v_mov_b32_dpp v130, v128 quad_perm:[2,3,0,1] row_mask:0xf bank_mask:0xf bound_ctrl:1
	v_mfma_f32_16x16x32_f16 v[140:143], v[18:21], v[124:127], v[92:95]
	v_mov_b32_dpp v131, v128 quad_perm:[3,0,1,2] row_mask:0xf bank_mask:0xf bound_ctrl:1
	s_nop 1
	v_mfma_f32_16x16x32_f16 v[132:135], v[2:5], v[128:131], v[132:135]
	v_fma_f32 v154, v56, v150, v58
	v_fma_f32 v155, v57, v151, v59
	v_mfma_f32_16x16x32_f16 v[136:139], v[14:17], v[128:131], v[136:139]
	v_fma_f32 v152, v50, v148, v52
	v_fma_f32 v153, v51, v149, v53
	v_mfma_f32_16x16x32_f16 v[140:143], v[22:25], v[128:131], v[140:143]
	ds_write_b32 v164, v124 offset:20064
	ds_write_b32 v164, v128 offset:20068
	s_nop 2
	v_cndmask_b32_e64 v160, v136, v132, s[6:7]
	v_cndmask_b32_e64 v161, v137, v133, s[6:7]
	v_cndmask_b32_e64 v162, v138, v134, s[6:7]
	v_cndmask_b32_e64 v163, v139, v135, s[6:7]
	v_cndmask_b32_e64 v156, v140, v160, s[4:5]
	v_cndmask_b32_e64 v157, v141, v161, s[4:5]
	v_exp_f32_e32 v156, v156
	v_exp_f32_e32 v157, v157
	v_cndmask_b32_e64 v158, v142, v162, s[4:5]
	v_cndmask_b32_e64 v159, v143, v163, s[4:5]
	v_pk_add_f32 v[156:157], v[156:157], 1.0 op_sel_hi:[1,0]
	v_exp_f32_e32 v158, v158
	v_rcp_f32_e32 v156, v156
	v_rcp_f32_e32 v157, v157
	v_exp_f32_e32 v159, v159
	v_pk_fma_f32 v[148:149], v[54:55], v[156:157], v[152:153]
	v_pk_add_f32 v[158:159], v[158:159], 1.0 op_sel_hi:[1,0]
	v_cvt_pk_f16_f32 v124, v148, v149
	v_rcp_f32_e32 v158, v158
	v_rcp_f32_e32 v159, v159
	v_mov_b32_dpp v125, v124 quad_perm:[1,2,3,0] row_mask:0xf bank_mask:0xf bound_ctrl:1
	v_mov_b32_dpp v126, v124 quad_perm:[2,3,0,1] row_mask:0xf bank_mask:0xf bound_ctrl:1
	v_mov_b32_dpp v127, v124 quad_perm:[3,0,1,2] row_mask:0xf bank_mask:0xf bound_ctrl:1
	v_pk_fma_f32 v[150:151], v[60:61], v[158:159], v[154:155]
	s_waitcnt lgkmcnt(15)
	v_mfma_f32_16x16x32_f16 v[132:135], v[6:9], v[124:127], v[96:99]
	v_cvt_pk_f16_f32 v128, v150, v151
	s_nop 0
	v_mfma_f32_16x16x32_f16 v[136:139], v[10:13], v[124:127], v[96:99]
	v_mov_b32_dpp v129, v128 quad_perm:[1,2,3,0] row_mask:0xf bank_mask:0xf bound_ctrl:1
	v_mov_b32_dpp v130, v128 quad_perm:[2,3,0,1] row_mask:0xf bank_mask:0xf bound_ctrl:1
	v_mfma_f32_16x16x32_f16 v[140:143], v[18:21], v[124:127], v[96:99]
	v_mov_b32_dpp v131, v128 quad_perm:[3,0,1,2] row_mask:0xf bank_mask:0xf bound_ctrl:1
	s_nop 1
	v_mfma_f32_16x16x32_f16 v[132:135], v[2:5], v[128:131], v[132:135]
	v_fma_f32 v154, v56, v150, v58
	v_fma_f32 v155, v57, v151, v59
	v_mfma_f32_16x16x32_f16 v[136:139], v[14:17], v[128:131], v[136:139]
	v_fma_f32 v152, v50, v148, v52
	v_fma_f32 v153, v51, v149, v53
	v_mfma_f32_16x16x32_f16 v[140:143], v[22:25], v[128:131], v[140:143]
	ds_write_b32 v164, v124 offset:20592
	ds_write_b32 v164, v128 offset:20596
	s_nop 2
	v_cndmask_b32_e64 v160, v136, v132, s[6:7]
	v_cndmask_b32_e64 v161, v137, v133, s[6:7]
	v_cndmask_b32_e64 v162, v138, v134, s[6:7]
	v_cndmask_b32_e64 v163, v139, v135, s[6:7]
	v_cndmask_b32_e64 v156, v140, v160, s[4:5]
	v_cndmask_b32_e64 v157, v141, v161, s[4:5]
	v_exp_f32_e32 v156, v156
	v_exp_f32_e32 v157, v157
	v_cndmask_b32_e64 v158, v142, v162, s[4:5]
	v_cndmask_b32_e64 v159, v143, v163, s[4:5]
	v_pk_add_f32 v[156:157], v[156:157], 1.0 op_sel_hi:[1,0]
	v_exp_f32_e32 v158, v158
	v_rcp_f32_e32 v156, v156
	v_rcp_f32_e32 v157, v157
	v_exp_f32_e32 v159, v159
	v_pk_fma_f32 v[148:149], v[54:55], v[156:157], v[152:153]
	v_pk_add_f32 v[158:159], v[158:159], 1.0 op_sel_hi:[1,0]
	v_cvt_pk_f16_f32 v124, v148, v149
	v_rcp_f32_e32 v158, v158
	v_rcp_f32_e32 v159, v159
	v_mov_b32_dpp v125, v124 quad_perm:[1,2,3,0] row_mask:0xf bank_mask:0xf bound_ctrl:1
	v_mov_b32_dpp v126, v124 quad_perm:[2,3,0,1] row_mask:0xf bank_mask:0xf bound_ctrl:1
	v_mov_b32_dpp v127, v124 quad_perm:[3,0,1,2] row_mask:0xf bank_mask:0xf bound_ctrl:1
	v_pk_fma_f32 v[150:151], v[60:61], v[158:159], v[154:155]
	s_waitcnt lgkmcnt(15)
	v_mfma_f32_16x16x32_f16 v[132:135], v[6:9], v[124:127], v[100:103]
	v_cvt_pk_f16_f32 v128, v150, v151
	s_nop 0
	v_mfma_f32_16x16x32_f16 v[136:139], v[10:13], v[124:127], v[100:103]
	v_mov_b32_dpp v129, v128 quad_perm:[1,2,3,0] row_mask:0xf bank_mask:0xf bound_ctrl:1
	v_mov_b32_dpp v130, v128 quad_perm:[2,3,0,1] row_mask:0xf bank_mask:0xf bound_ctrl:1
	v_mfma_f32_16x16x32_f16 v[140:143], v[18:21], v[124:127], v[100:103]
	v_mov_b32_dpp v131, v128 quad_perm:[3,0,1,2] row_mask:0xf bank_mask:0xf bound_ctrl:1
	s_nop 1
	v_mfma_f32_16x16x32_f16 v[132:135], v[2:5], v[128:131], v[132:135]
	v_fma_f32 v154, v56, v150, v58
	v_fma_f32 v155, v57, v151, v59
	v_mfma_f32_16x16x32_f16 v[136:139], v[14:17], v[128:131], v[136:139]
	v_fma_f32 v152, v50, v148, v52
	v_fma_f32 v153, v51, v149, v53
	v_mfma_f32_16x16x32_f16 v[140:143], v[22:25], v[128:131], v[140:143]
	ds_write_b32 v164, v124 offset:21120
	ds_write_b32 v164, v128 offset:21124
	s_nop 2
	v_cndmask_b32_e64 v160, v136, v132, s[6:7]
	v_cndmask_b32_e64 v161, v137, v133, s[6:7]
	v_cndmask_b32_e64 v162, v138, v134, s[6:7]
	v_cndmask_b32_e64 v163, v139, v135, s[6:7]
	v_cndmask_b32_e64 v156, v140, v160, s[4:5]
	v_cndmask_b32_e64 v157, v141, v161, s[4:5]
	v_exp_f32_e32 v156, v156
	v_exp_f32_e32 v157, v157
	v_cndmask_b32_e64 v158, v142, v162, s[4:5]
	v_cndmask_b32_e64 v159, v143, v163, s[4:5]
	v_pk_add_f32 v[156:157], v[156:157], 1.0 op_sel_hi:[1,0]
	v_exp_f32_e32 v158, v158
	v_rcp_f32_e32 v156, v156
	v_rcp_f32_e32 v157, v157
	v_exp_f32_e32 v159, v159
	v_pk_fma_f32 v[148:149], v[54:55], v[156:157], v[152:153]
	v_pk_add_f32 v[158:159], v[158:159], 1.0 op_sel_hi:[1,0]
	v_cvt_pk_f16_f32 v124, v148, v149
	v_rcp_f32_e32 v158, v158
	v_rcp_f32_e32 v159, v159
	v_mov_b32_dpp v125, v124 quad_perm:[1,2,3,0] row_mask:0xf bank_mask:0xf bound_ctrl:1
	v_mov_b32_dpp v126, v124 quad_perm:[2,3,0,1] row_mask:0xf bank_mask:0xf bound_ctrl:1
	v_mov_b32_dpp v127, v124 quad_perm:[3,0,1,2] row_mask:0xf bank_mask:0xf bound_ctrl:1
	v_pk_fma_f32 v[150:151], v[60:61], v[158:159], v[154:155]
	s_waitcnt lgkmcnt(15)
	v_mfma_f32_16x16x32_f16 v[132:135], v[6:9], v[124:127], v[104:107]
	v_cvt_pk_f16_f32 v128, v150, v151
	s_nop 0
	v_mfma_f32_16x16x32_f16 v[136:139], v[10:13], v[124:127], v[104:107]
	v_mov_b32_dpp v129, v128 quad_perm:[1,2,3,0] row_mask:0xf bank_mask:0xf bound_ctrl:1
	v_mov_b32_dpp v130, v128 quad_perm:[2,3,0,1] row_mask:0xf bank_mask:0xf bound_ctrl:1
	v_mfma_f32_16x16x32_f16 v[140:143], v[18:21], v[124:127], v[104:107]
	v_mov_b32_dpp v131, v128 quad_perm:[3,0,1,2] row_mask:0xf bank_mask:0xf bound_ctrl:1
	s_nop 1
	v_mfma_f32_16x16x32_f16 v[132:135], v[2:5], v[128:131], v[132:135]
	v_fma_f32 v154, v56, v150, v58
	v_fma_f32 v155, v57, v151, v59
	v_mfma_f32_16x16x32_f16 v[136:139], v[14:17], v[128:131], v[136:139]
	v_fma_f32 v152, v50, v148, v52
	v_fma_f32 v153, v51, v149, v53
	v_mfma_f32_16x16x32_f16 v[140:143], v[22:25], v[128:131], v[140:143]
	ds_write_b32 v164, v124 offset:21648
	ds_write_b32 v164, v128 offset:21652
	s_nop 2
	v_cndmask_b32_e64 v160, v136, v132, s[6:7]
	v_cndmask_b32_e64 v161, v137, v133, s[6:7]
	v_cndmask_b32_e64 v162, v138, v134, s[6:7]
	v_cndmask_b32_e64 v163, v139, v135, s[6:7]
	v_cndmask_b32_e64 v156, v140, v160, s[4:5]
	v_cndmask_b32_e64 v157, v141, v161, s[4:5]
	v_exp_f32_e32 v156, v156
	v_exp_f32_e32 v157, v157
	v_cndmask_b32_e64 v158, v142, v162, s[4:5]
	v_cndmask_b32_e64 v159, v143, v163, s[4:5]
	v_pk_add_f32 v[156:157], v[156:157], 1.0 op_sel_hi:[1,0]
	v_exp_f32_e32 v158, v158
	v_rcp_f32_e32 v156, v156
	v_rcp_f32_e32 v157, v157
	v_exp_f32_e32 v159, v159
	v_pk_fma_f32 v[148:149], v[54:55], v[156:157], v[152:153]
	v_pk_add_f32 v[158:159], v[158:159], 1.0 op_sel_hi:[1,0]
	v_cvt_pk_f16_f32 v124, v148, v149
	v_rcp_f32_e32 v158, v158
	v_rcp_f32_e32 v159, v159
	v_mov_b32_dpp v125, v124 quad_perm:[1,2,3,0] row_mask:0xf bank_mask:0xf bound_ctrl:1
	v_mov_b32_dpp v126, v124 quad_perm:[2,3,0,1] row_mask:0xf bank_mask:0xf bound_ctrl:1
	v_mov_b32_dpp v127, v124 quad_perm:[3,0,1,2] row_mask:0xf bank_mask:0xf bound_ctrl:1
	v_pk_fma_f32 v[150:151], v[60:61], v[158:159], v[154:155]
	s_waitcnt lgkmcnt(15)
	v_mfma_f32_16x16x32_f16 v[132:135], v[6:9], v[124:127], v[108:111]
	v_cvt_pk_f16_f32 v128, v150, v151
	s_nop 0
	v_mfma_f32_16x16x32_f16 v[136:139], v[10:13], v[124:127], v[108:111]
	v_mov_b32_dpp v129, v128 quad_perm:[1,2,3,0] row_mask:0xf bank_mask:0xf bound_ctrl:1
	v_mov_b32_dpp v130, v128 quad_perm:[2,3,0,1] row_mask:0xf bank_mask:0xf bound_ctrl:1
	v_mfma_f32_16x16x32_f16 v[140:143], v[18:21], v[124:127], v[108:111]
	v_mov_b32_dpp v131, v128 quad_perm:[3,0,1,2] row_mask:0xf bank_mask:0xf bound_ctrl:1
	s_nop 1
	v_mfma_f32_16x16x32_f16 v[132:135], v[2:5], v[128:131], v[132:135]
	v_fma_f32 v154, v56, v150, v58
	v_fma_f32 v155, v57, v151, v59
	v_mfma_f32_16x16x32_f16 v[136:139], v[14:17], v[128:131], v[136:139]
	v_fma_f32 v152, v50, v148, v52
	v_fma_f32 v153, v51, v149, v53
	v_mfma_f32_16x16x32_f16 v[140:143], v[22:25], v[128:131], v[140:143]
	ds_write_b32 v164, v124 offset:22176
	ds_write_b32 v164, v128 offset:22180
	s_nop 2
	v_cndmask_b32_e64 v160, v136, v132, s[6:7]
	v_cndmask_b32_e64 v161, v137, v133, s[6:7]
	v_cndmask_b32_e64 v162, v138, v134, s[6:7]
	v_cndmask_b32_e64 v163, v139, v135, s[6:7]
	v_cndmask_b32_e64 v156, v140, v160, s[4:5]
	v_cndmask_b32_e64 v157, v141, v161, s[4:5]
	v_exp_f32_e32 v156, v156
	v_exp_f32_e32 v157, v157
	v_cndmask_b32_e64 v158, v142, v162, s[4:5]
	v_cndmask_b32_e64 v159, v143, v163, s[4:5]
	v_pk_add_f32 v[156:157], v[156:157], 1.0 op_sel_hi:[1,0]
	v_exp_f32_e32 v158, v158
	v_rcp_f32_e32 v156, v156
	v_rcp_f32_e32 v157, v157
	v_exp_f32_e32 v159, v159
	v_pk_fma_f32 v[148:149], v[54:55], v[156:157], v[152:153]
	v_pk_add_f32 v[158:159], v[158:159], 1.0 op_sel_hi:[1,0]
	v_cvt_pk_f16_f32 v124, v148, v149
	v_rcp_f32_e32 v158, v158
	v_rcp_f32_e32 v159, v159
	v_mov_b32_dpp v125, v124 quad_perm:[1,2,3,0] row_mask:0xf bank_mask:0xf bound_ctrl:1
	v_mov_b32_dpp v126, v124 quad_perm:[2,3,0,1] row_mask:0xf bank_mask:0xf bound_ctrl:1
	v_mov_b32_dpp v127, v124 quad_perm:[3,0,1,2] row_mask:0xf bank_mask:0xf bound_ctrl:1
	v_pk_fma_f32 v[150:151], v[60:61], v[158:159], v[154:155]
	s_waitcnt lgkmcnt(15)
	v_mfma_f32_16x16x32_f16 v[132:135], v[6:9], v[124:127], v[112:115]
	v_cvt_pk_f16_f32 v128, v150, v151
	s_nop 0
	v_mfma_f32_16x16x32_f16 v[136:139], v[10:13], v[124:127], v[112:115]
	v_mov_b32_dpp v129, v128 quad_perm:[1,2,3,0] row_mask:0xf bank_mask:0xf bound_ctrl:1
	v_mov_b32_dpp v130, v128 quad_perm:[2,3,0,1] row_mask:0xf bank_mask:0xf bound_ctrl:1
	v_mfma_f32_16x16x32_f16 v[140:143], v[18:21], v[124:127], v[112:115]
	v_mov_b32_dpp v131, v128 quad_perm:[3,0,1,2] row_mask:0xf bank_mask:0xf bound_ctrl:1
	s_nop 1
	v_mfma_f32_16x16x32_f16 v[132:135], v[2:5], v[128:131], v[132:135]
	v_fma_f32 v154, v56, v150, v58
	v_fma_f32 v155, v57, v151, v59
	v_mfma_f32_16x16x32_f16 v[136:139], v[14:17], v[128:131], v[136:139]
	v_fma_f32 v152, v50, v148, v52
	v_fma_f32 v153, v51, v149, v53
	v_mfma_f32_16x16x32_f16 v[140:143], v[22:25], v[128:131], v[140:143]
	ds_write_b32 v164, v124 offset:22704
	ds_write_b32 v164, v128 offset:22708
	s_nop 2
	v_cndmask_b32_e64 v160, v136, v132, s[6:7]
	v_cndmask_b32_e64 v161, v137, v133, s[6:7]
	v_cndmask_b32_e64 v162, v138, v134, s[6:7]
	v_cndmask_b32_e64 v163, v139, v135, s[6:7]
	v_cndmask_b32_e64 v156, v140, v160, s[4:5]
	v_cndmask_b32_e64 v157, v141, v161, s[4:5]
	v_exp_f32_e32 v156, v156
	v_exp_f32_e32 v157, v157
	v_cndmask_b32_e64 v158, v142, v162, s[4:5]
	v_cndmask_b32_e64 v159, v143, v163, s[4:5]
	v_pk_add_f32 v[156:157], v[156:157], 1.0 op_sel_hi:[1,0]
	v_exp_f32_e32 v158, v158
	v_rcp_f32_e32 v156, v156
	v_rcp_f32_e32 v157, v157
	v_exp_f32_e32 v159, v159
	v_pk_fma_f32 v[148:149], v[54:55], v[156:157], v[152:153]
	v_pk_add_f32 v[158:159], v[158:159], 1.0 op_sel_hi:[1,0]
	v_cvt_pk_f16_f32 v124, v148, v149
	v_rcp_f32_e32 v158, v158
	v_rcp_f32_e32 v159, v159
	v_mov_b32_dpp v125, v124 quad_perm:[1,2,3,0] row_mask:0xf bank_mask:0xf bound_ctrl:1
	v_mov_b32_dpp v126, v124 quad_perm:[2,3,0,1] row_mask:0xf bank_mask:0xf bound_ctrl:1
	v_mov_b32_dpp v127, v124 quad_perm:[3,0,1,2] row_mask:0xf bank_mask:0xf bound_ctrl:1
	v_pk_fma_f32 v[150:151], v[60:61], v[158:159], v[154:155]
	s_waitcnt lgkmcnt(15)
	v_mfma_f32_16x16x32_f16 v[132:135], v[6:9], v[124:127], v[116:119]
	v_cvt_pk_f16_f32 v128, v150, v151
	s_nop 0
	v_mfma_f32_16x16x32_f16 v[136:139], v[10:13], v[124:127], v[116:119]
	v_mov_b32_dpp v129, v128 quad_perm:[1,2,3,0] row_mask:0xf bank_mask:0xf bound_ctrl:1
	v_mov_b32_dpp v130, v128 quad_perm:[2,3,0,1] row_mask:0xf bank_mask:0xf bound_ctrl:1
	v_mfma_f32_16x16x32_f16 v[140:143], v[18:21], v[124:127], v[116:119]
	v_mov_b32_dpp v131, v128 quad_perm:[3,0,1,2] row_mask:0xf bank_mask:0xf bound_ctrl:1
	s_nop 1
	v_mfma_f32_16x16x32_f16 v[132:135], v[2:5], v[128:131], v[132:135]
	v_fma_f32 v154, v56, v150, v58
	v_fma_f32 v155, v57, v151, v59
	v_mfma_f32_16x16x32_f16 v[136:139], v[14:17], v[128:131], v[136:139]
	v_fma_f32 v152, v50, v148, v52
	v_fma_f32 v153, v51, v149, v53
	v_mfma_f32_16x16x32_f16 v[140:143], v[22:25], v[128:131], v[140:143]
	ds_write_b32 v164, v124 offset:23232
	ds_write_b32 v164, v128 offset:23236
	s_nop 2
	v_cndmask_b32_e64 v160, v136, v132, s[6:7]
	v_cndmask_b32_e64 v161, v137, v133, s[6:7]
	v_cndmask_b32_e64 v162, v138, v134, s[6:7]
	v_cndmask_b32_e64 v163, v139, v135, s[6:7]
	v_cndmask_b32_e64 v156, v140, v160, s[4:5]
	v_cndmask_b32_e64 v157, v141, v161, s[4:5]
	v_exp_f32_e32 v156, v156
	v_exp_f32_e32 v157, v157
	v_cndmask_b32_e64 v158, v142, v162, s[4:5]
	v_cndmask_b32_e64 v159, v143, v163, s[4:5]
	v_pk_add_f32 v[156:157], v[156:157], 1.0 op_sel_hi:[1,0]
	v_exp_f32_e32 v158, v158
	v_rcp_f32_e32 v156, v156
	v_rcp_f32_e32 v157, v157
	v_exp_f32_e32 v159, v159
	v_pk_fma_f32 v[148:149], v[54:55], v[156:157], v[152:153]
	v_pk_add_f32 v[158:159], v[158:159], 1.0 op_sel_hi:[1,0]
	v_cvt_pk_f16_f32 v124, v148, v149
	v_rcp_f32_e32 v158, v158
	v_rcp_f32_e32 v159, v159
	v_mov_b32_dpp v125, v124 quad_perm:[1,2,3,0] row_mask:0xf bank_mask:0xf bound_ctrl:1
	v_mov_b32_dpp v126, v124 quad_perm:[2,3,0,1] row_mask:0xf bank_mask:0xf bound_ctrl:1
	v_mov_b32_dpp v127, v124 quad_perm:[3,0,1,2] row_mask:0xf bank_mask:0xf bound_ctrl:1
	v_pk_fma_f32 v[150:151], v[60:61], v[158:159], v[154:155]
	s_waitcnt lgkmcnt(15)
	v_mfma_f32_16x16x32_f16 v[132:135], v[6:9], v[124:127], v[120:123]
	v_cvt_pk_f16_f32 v128, v150, v151
	s_nop 0
	v_mfma_f32_16x16x32_f16 v[136:139], v[10:13], v[124:127], v[120:123]
	v_mov_b32_dpp v129, v128 quad_perm:[1,2,3,0] row_mask:0xf bank_mask:0xf bound_ctrl:1
	v_mov_b32_dpp v130, v128 quad_perm:[2,3,0,1] row_mask:0xf bank_mask:0xf bound_ctrl:1
	v_mfma_f32_16x16x32_f16 v[140:143], v[18:21], v[124:127], v[120:123]
	v_mov_b32_dpp v131, v128 quad_perm:[3,0,1,2] row_mask:0xf bank_mask:0xf bound_ctrl:1
	s_nop 1
	v_mfma_f32_16x16x32_f16 v[132:135], v[2:5], v[128:131], v[132:135]
	v_fma_f32 v154, v56, v150, v58
	v_fma_f32 v155, v57, v151, v59
	v_mfma_f32_16x16x32_f16 v[136:139], v[14:17], v[128:131], v[136:139]
	v_fma_f32 v152, v50, v148, v52
	v_fma_f32 v153, v51, v149, v53
	v_mfma_f32_16x16x32_f16 v[140:143], v[22:25], v[128:131], v[140:143]
	ds_write_b32 v164, v124 offset:23760
	ds_write_b32 v164, v128 offset:23764
	s_nop 2
	v_cndmask_b32_e64 v160, v136, v132, s[6:7]
	v_cndmask_b32_e64 v161, v137, v133, s[6:7]
	v_cndmask_b32_e64 v162, v138, v134, s[6:7]
	v_cndmask_b32_e64 v163, v139, v135, s[6:7]
	v_cndmask_b32_e64 v156, v140, v160, s[4:5]
	v_cndmask_b32_e64 v157, v141, v161, s[4:5]
	v_exp_f32_e32 v156, v156
	v_exp_f32_e32 v157, v157
	v_cndmask_b32_e64 v158, v142, v162, s[4:5]
	v_cndmask_b32_e64 v159, v143, v163, s[4:5]
	v_pk_add_f32 v[156:157], v[156:157], 1.0 op_sel_hi:[1,0]
	v_exp_f32_e32 v158, v158
	v_rcp_f32_e32 v156, v156
	v_rcp_f32_e32 v157, v157
	v_exp_f32_e32 v159, v159
	v_pk_fma_f32 v[148:149], v[54:55], v[156:157], v[152:153]
	v_pk_add_f32 v[158:159], v[158:159], 1.0 op_sel_hi:[1,0]
	v_cvt_pk_f16_f32 v124, v148, v149
	v_rcp_f32_e32 v158, v158
	v_rcp_f32_e32 v159, v159
	v_mov_b32_dpp v125, v124 quad_perm:[1,2,3,0] row_mask:0xf bank_mask:0xf bound_ctrl:1
	v_mov_b32_dpp v126, v124 quad_perm:[2,3,0,1] row_mask:0xf bank_mask:0xf bound_ctrl:1
	v_mov_b32_dpp v127, v124 quad_perm:[3,0,1,2] row_mask:0xf bank_mask:0xf bound_ctrl:1
	v_pk_fma_f32 v[150:151], v[60:61], v[158:159], v[154:155]
	s_waitcnt lgkmcnt(15)
	v_mfma_f32_16x16x32_f16 v[132:135], v[6:9], v[124:127], v[44:47]
	v_cvt_pk_f16_f32 v128, v150, v151
	s_nop 0
	v_mfma_f32_16x16x32_f16 v[136:139], v[10:13], v[124:127], v[44:47]
	v_mov_b32_dpp v129, v128 quad_perm:[1,2,3,0] row_mask:0xf bank_mask:0xf bound_ctrl:1
	v_mov_b32_dpp v130, v128 quad_perm:[2,3,0,1] row_mask:0xf bank_mask:0xf bound_ctrl:1
	v_mfma_f32_16x16x32_f16 v[140:143], v[18:21], v[124:127], v[44:47]
	v_mov_b32_dpp v131, v128 quad_perm:[3,0,1,2] row_mask:0xf bank_mask:0xf bound_ctrl:1
	s_nop 1
	v_mfma_f32_16x16x32_f16 v[132:135], v[2:5], v[128:131], v[132:135]
	v_fma_f32 v154, v56, v150, v58
	v_fma_f32 v155, v57, v151, v59
	v_mfma_f32_16x16x32_f16 v[136:139], v[14:17], v[128:131], v[136:139]
	v_fma_f32 v152, v50, v148, v52
	v_fma_f32 v153, v51, v149, v53
	v_mfma_f32_16x16x32_f16 v[140:143], v[22:25], v[128:131], v[140:143]
	ds_write_b32 v164, v124 offset:24288
	ds_write_b32 v164, v128 offset:24292
	s_nop 2
	v_cndmask_b32_e64 v160, v136, v132, s[6:7]
	v_cndmask_b32_e64 v161, v137, v133, s[6:7]
	v_cndmask_b32_e64 v162, v138, v134, s[6:7]
	v_cndmask_b32_e64 v163, v139, v135, s[6:7]
	v_cndmask_b32_e64 v156, v140, v160, s[4:5]
	v_cndmask_b32_e64 v157, v141, v161, s[4:5]
	v_exp_f32_e32 v156, v156
	v_exp_f32_e32 v157, v157
	v_cndmask_b32_e64 v158, v142, v162, s[4:5]
	v_cndmask_b32_e64 v159, v143, v163, s[4:5]
	v_pk_add_f32 v[156:157], v[156:157], 1.0 op_sel_hi:[1,0]
	v_exp_f32_e32 v158, v158
	v_rcp_f32_e32 v156, v156
	v_rcp_f32_e32 v157, v157
	v_exp_f32_e32 v159, v159
	v_pk_fma_f32 v[148:149], v[54:55], v[156:157], v[152:153]
	v_pk_add_f32 v[158:159], v[158:159], 1.0 op_sel_hi:[1,0]
	v_cvt_pk_f16_f32 v124, v148, v149
	v_rcp_f32_e32 v158, v158
	v_rcp_f32_e32 v159, v159
	v_mov_b32_dpp v125, v124 quad_perm:[1,2,3,0] row_mask:0xf bank_mask:0xf bound_ctrl:1
	v_mov_b32_dpp v126, v124 quad_perm:[2,3,0,1] row_mask:0xf bank_mask:0xf bound_ctrl:1
	v_mov_b32_dpp v127, v124 quad_perm:[3,0,1,2] row_mask:0xf bank_mask:0xf bound_ctrl:1
	v_pk_fma_f32 v[150:151], v[60:61], v[158:159], v[154:155]
	s_nop 0
	v_mfma_f32_16x16x32_f16 v[132:135], v[6:9], v[124:127], v[168:171]
	v_cvt_pk_f16_f32 v128, v150, v151
	s_nop 0
	v_mfma_f32_16x16x32_f16 v[136:139], v[10:13], v[124:127], v[168:171]
	v_mov_b32_dpp v129, v128 quad_perm:[1,2,3,0] row_mask:0xf bank_mask:0xf bound_ctrl:1
	v_mov_b32_dpp v130, v128 quad_perm:[2,3,0,1] row_mask:0xf bank_mask:0xf bound_ctrl:1
	v_mfma_f32_16x16x32_f16 v[140:143], v[18:21], v[124:127], v[168:171]
	v_mov_b32_dpp v131, v128 quad_perm:[3,0,1,2] row_mask:0xf bank_mask:0xf bound_ctrl:1
	ds_write_b32 v164, v124 offset:24816
	ds_write_b32 v164, v128 offset:24820
	s_waitcnt lgkmcnt(0)
	s_barrier
	s_add_i32 s3, s3, 1
	v_mfma_f32_16x16x32_f16 v[132:135], v[2:5], v[128:131], v[132:135]
	v_fma_f32 v154, v56, v150, v58
	v_fma_f32 v155, v57, v151, v59
	v_mfma_f32_16x16x32_f16 v[136:139], v[14:17], v[128:131], v[136:139]
	v_fma_f32 v152, v50, v148, v52
	v_fma_f32 v153, v51, v149, v53
	v_mfma_f32_16x16x32_f16 v[140:143], v[22:25], v[128:131], v[140:143]
	s_cmp_lt_u32 s3, 64
	s_cbranch_scc1 .LBB3_49
	s_branch .LBB3_48

	.amdhsa_kernel _Z10k_enc_scanPKDF16_PKfS2_S2_S2_S2_S2_S2_S2_S2_S2_S0_S2_S2_S2_S2_S2_S0_S2_PfPjS2_S2_S2_S2_S2_S2_S2_S2_S2_S2_S2_S2_PDF16_S5_S3_
		.amdhsa_group_segment_fixed_size 91136
		.amdhsa_private_segment_fixed_size 0
		.amdhsa_kernarg_size 288
		.amdhsa_user_sgpr_count 2
		.amdhsa_user_sgpr_dispatch_ptr 0
		.amdhsa_user_sgpr_queue_ptr 0
		.amdhsa_user_sgpr_kernarg_segment_ptr 1
		.amdhsa_user_sgpr_dispatch_id 0
		.amdhsa_user_sgpr_kernarg_preload_length 0
		.amdhsa_user_sgpr_kernarg_preload_offset 0
		.amdhsa_user_sgpr_private_segment_size 0
		.amdhsa_uses_dynamic_stack 0
		.amdhsa_enable_private_segment 0
		.amdhsa_system_sgpr_workgroup_id_x 1
		.amdhsa_system_sgpr_workgroup_id_y 0
		.amdhsa_system_sgpr_workgroup_id_z 0
		.amdhsa_system_sgpr_workgroup_info 0
		.amdhsa_system_vgpr_workitem_id 0
		.amdhsa_next_free_vgpr 208
		.amdhsa_next_free_sgpr 98
		.amdhsa_accum_offset 208
		.amdhsa_reserve_vcc 1
		.amdhsa_float_round_mode_32 0
		.amdhsa_float_round_mode_16_64 0
		.amdhsa_float_denorm_mode_32 3
		.amdhsa_float_denorm_mode_16_64 3
		.amdhsa_dx10_clamp 1
		.amdhsa_ieee_mode 1
		.amdhsa_fp16_overflow 0
		.amdhsa_tg_split 0
		.amdhsa_exception_fp_ieee_invalid_op 0
		.amdhsa_exception_fp_denorm_src 0
		.amdhsa_exception_fp_ieee_div_zero 0
		.amdhsa_exception_fp_ieee_overflow 0
		.amdhsa_exception_fp_ieee_underflow 0
		.amdhsa_exception_fp_ieee_inexact 0
		.amdhsa_exception_int_div_zero 0
	.end_amdhsa_kernel

amdhsa.kernels:
  - .agpr_count:     8
    .args:
      - .actual_access:  read_only
        .address_space:  global
        .offset:         0
        .size:           8
        .value_kind:     global_buffer
      - .actual_access:  read_only
        .address_space:  global
        .offset:         8
        .size:           8
        .value_kind:     global_buffer
      - .actual_access:  write_only
        .address_space:  global
        .offset:         16
        .size:           8
        .value_kind:     global_buffer
      - .actual_access:  write_only
        .address_space:  global
        .offset:         24
        .size:           8
        .value_kind:     global_buffer
      - .actual_access:  read_only
        .address_space:  global
        .offset:         32
        .size:           8
        .value_kind:     global_buffer
      - .actual_access:  read_only
        .address_space:  global
        .offset:         40
        .size:           8
        .value_kind:     global_buffer
      - .actual_access:  write_only
        .address_space:  global
        .offset:         48
        .size:           8
        .value_kind:     global_buffer
      - .actual_access:  write_only
        .address_space:  global
        .offset:         56
        .size:           8
        .value_kind:     global_buffer
      - .actual_access:  write_only
        .address_space:  global
        .offset:         64
        .size:           8
        .value_kind:     global_buffer
    .group_segment_fixed_size: 24976
    .kernarg_segment_align: 8
    .kernarg_segment_size: 72
    .language:       OpenCL C
    .language_version:
      - 2
      - 0
    .max_flat_workgroup_size: 256
    .name:           _Z9k_fb_mfmaPKfS0_PDF16_PfS0_S0_S1_S1_Pj
    .private_segment_fixed_size: 0
    .sgpr_count:     24
    .sgpr_spill_count: 0
    .symbol:         _Z9k_fb_mfmaPKfS0_PDF16_PfS0_S0_S1_S1_Pj.kd
    .uniform_work_group_size: 1
    .uses_dynamic_stack: false
    .vgpr_count:     92
    .vgpr_spill_count: 0
    .wavefront_size: 64
  - .agpr_count:     0
    .args:
      - .actual_access:  read_only
        .address_space:  global
        .offset:         0
        .size:           8
        .value_kind:     global_buffer
      - .actual_access:  read_only
        .address_space:  global
        .offset:         8
        .size:           8
        .value_kind:     global_buffer
      - .actual_access:  write_only
        .address_space:  global
        .offset:         16
        .size:           8
        .value_kind:     global_buffer
      - .actual_access:  write_only
        .address_space:  global
        .offset:         24
        .size:           8
        .value_kind:     global_buffer
    .group_segment_fixed_size: 0
    .kernarg_segment_align: 8
    .kernarg_segment_size: 32
    .language:       OpenCL C
    .language_version:
      - 2
      - 0
    .max_flat_workgroup_size: 1024
    .name:           _Z6k_prepPKfS0_PDF16_S1_
    .private_segment_fixed_size: 0
    .sgpr_count:     19
    .sgpr_spill_count: 0
    .symbol:         _Z6k_prepPKfS0_PDF16_S1_.kd
    .uniform_work_group_size: 1
    .uses_dynamic_stack: false
    .vgpr_count:     8
    .vgpr_spill_count: 0
    .wavefront_size: 64
  - .agpr_count:     0
    .args:
      - .actual_access:  read_only
        .address_space:  global
        .offset:         0
        .size:           8
        .value_kind:     global_buffer
      - .actual_access:  read_only
        .address_space:  global
        .offset:         8
        .size:           8
        .value_kind:     global_buffer
      - .actual_access:  read_only
        .address_space:  global
        .offset:         16
        .size:           8
        .value_kind:     global_buffer
      - .actual_access:  read_only
        .address_space:  global
        .offset:         24
        .size:           8
        .value_kind:     global_buffer
      - .actual_access:  read_only
        .address_space:  global
        .offset:         32
        .size:           8
        .value_kind:     global_buffer
      - .actual_access:  read_only
        .address_space:  global
        .offset:         40
        .size:           8
        .value_kind:     global_buffer
      - .actual_access:  read_only
        .address_space:  global
        .offset:         48
        .size:           8
        .value_kind:     global_buffer
      - .actual_access:  read_only
        .address_space:  global
        .offset:         56
        .size:           8
        .value_kind:     global_buffer
      - .actual_access:  read_only
        .address_space:  global
        .offset:         64
        .size:           8
        .value_kind:     global_buffer
      - .actual_access:  read_only
        .address_space:  global
        .offset:         72
        .size:           8
        .value_kind:     global_buffer
      - .actual_access:  write_only
        .address_space:  global
        .offset:         80
        .size:           8
        .value_kind:     global_buffer
      - .actual_access:  write_only
        .address_space:  global
        .offset:         88
        .size:           8
        .value_kind:     global_buffer
    .group_segment_fixed_size: 236
    .kernarg_segment_align: 8
    .kernarg_segment_size: 96
    .language:       OpenCL C
    .language_version:
      - 2
      - 0
    .max_flat_workgroup_size: 192
    .name:           _Z6k_gatePKfS0_S0_S0_S0_S0_S0_S0_S0_S0_PfPj
    .private_segment_fixed_size: 0
    .sgpr_count:     32
    .sgpr_spill_count: 0
    .symbol:         _Z6k_gatePKfS0_S0_S0_S0_S0_S0_S0_S0_S0_PfPj.kd
    .uniform_work_group_size: 1
    .uses_dynamic_stack: false
    .vgpr_count:     47
    .vgpr_spill_count: 0
    .wavefront_size: 64
  - .agpr_count:     0
    .args:
      - .actual_access:  read_only
        .address_space:  global
        .offset:         0
        .size:           8
        .value_kind:     global_buffer
      - .actual_access:  read_only
        .address_space:  global
        .offset:         8
        .size:           8
        .value_kind:     global_buffer
      - .actual_access:  read_only
        .address_space:  global
        .offset:         16
        .size:           8
        .value_kind:     global_buffer
      - .actual_access:  read_only
        .address_space:  global
        .offset:         24
        .size:           8
        .value_kind:     global_buffer
      - .actual_access:  read_only
        .address_space:  global
        .offset:         32
        .size:           8
        .value_kind:     global_buffer
      - .actual_access:  read_only
        .address_space:  global
        .offset:         40
        .size:           8
        .value_kind:     global_buffer
      - .actual_access:  read_only
        .address_space:  global
        .offset:         48
        .size:           8
        .value_kind:     global_buffer
      - .actual_access:  read_only
        .address_space:  global
        .offset:         56
        .size:           8
        .value_kind:     global_buffer
      - .actual_access:  read_only
        .address_space:  global
        .offset:         64
        .size:           8
        .value_kind:     global_buffer
      - .actual_access:  read_only
        .address_space:  global
        .offset:         72
        .size:           8
        .value_kind:     global_buffer
      - .actual_access:  read_only
        .address_space:  global
        .offset:         80
        .size:           8
        .value_kind:     global_buffer
      - .actual_access:  read_only
        .address_space:  global
        .offset:         88
        .size:           8
        .value_kind:     global_buffer
      - .actual_access:  read_only
        .address_space:  global
        .offset:         96
        .size:           8
        .value_kind:     global_buffer
      - .actual_access:  read_only
        .address_space:  global
        .offset:         104
        .size:           8
        .value_kind:     global_buffer
      - .actual_access:  read_only
        .address_space:  global
        .offset:         112
        .size:           8
        .value_kind:     global_buffer
      - .actual_access:  read_only
        .address_space:  global
        .offset:         120
        .size:           8
        .value_kind:     global_buffer
      - .actual_access:  read_only
        .address_space:  global
        .offset:         128
        .size:           8
        .value_kind:     global_buffer
      - .actual_access:  read_only
        .address_space:  global
        .offset:         136
        .size:           8
        .value_kind:     global_buffer
      - .actual_access:  read_only
        .address_space:  global
        .offset:         144
        .size:           8
        .value_kind:     global_buffer
      - .address_space:  global
        .offset:         152
        .size:           8
        .value_kind:     global_buffer
      - .address_space:  global
        .offset:         160
        .size:           8
        .value_kind:     global_buffer
      - .actual_access:  read_only
        .address_space:  global
        .offset:         168
        .size:           8
        .value_kind:     global_buffer
      - .actual_access:  read_only
        .address_space:  global
        .offset:         176
        .size:           8
        .value_kind:     global_buffer
      - .actual_access:  read_only
        .address_space:  global
        .offset:         184
        .size:           8
        .value_kind:     global_buffer
      - .actual_access:  read_only
        .address_space:  global
        .offset:         192
        .size:           8
        .value_kind:     global_buffer
      - .actual_access:  read_only
        .address_space:  global
        .offset:         200
        .size:           8
        .value_kind:     global_buffer
      - .actual_access:  read_only
        .address_space:  global
        .offset:         208
        .size:           8
        .value_kind:     global_buffer
      - .actual_access:  read_only
        .address_space:  global
        .offset:         216
        .size:           8
        .value_kind:     global_buffer
      - .actual_access:  read_only
        .address_space:  global
        .offset:         224
        .size:           8
        .value_kind:     global_buffer
      - .actual_access:  read_only
        .address_space:  global
        .offset:         232
        .size:           8
        .value_kind:     global_buffer
      - .actual_access:  read_only
        .address_space:  global
        .offset:         240
        .size:           8
        .value_kind:     global_buffer
      - .actual_access:  read_only
        .address_space:  global
        .offset:         248
        .size:           8
        .value_kind:     global_buffer
      - .actual_access:  read_only
        .address_space:  global
        .offset:         256
        .size:           8
        .value_kind:     global_buffer
      - .actual_access:  write_only
        .address_space:  global
        .offset:         264
        .size:           8
        .value_kind:     global_buffer
      - .actual_access:  write_only
        .address_space:  global
        .offset:         272
        .size:           8
        .value_kind:     global_buffer
      - .actual_access:  write_only
        .address_space:  global
        .offset:         280
        .size:           8
        .value_kind:     global_buffer
    .group_segment_fixed_size: 91136
    .kernarg_segment_align: 8
    .kernarg_segment_size: 288
    .language:       OpenCL C
    .language_version:
      - 2
      - 0
    .max_flat_workgroup_size: 320
    .name:           _Z10k_enc_scanPKDF16_PKfS2_S2_S2_S2_S2_S2_S2_S2_S2_S0_S2_S2_S2_S2_S2_S0_S2_PfPjS2_S2_S2_S2_S2_S2_S2_S2_S2_S2_S2_S2_PDF16_S5_S3_
    .private_segment_fixed_size: 0
    .sgpr_count:     104
    .sgpr_spill_count: 0
    .symbol:         _Z10k_enc_scanPKDF16_PKfS2_S2_S2_S2_S2_S2_S2_S2_S2_S0_S2_S2_S2_S2_S2_S0_S2_PfPjS2_S2_S2_S2_S2_S2_S2_S2_S2_S2_S2_S2_PDF16_S5_S3_.kd
    .uniform_work_group_size: 1
    .uses_dynamic_stack: false
    .vgpr_count:     208
    .vgpr_spill_count: 0
    .wavefront_size: 64
  - .agpr_count:     0
    .args:
      - .actual_access:  read_only
        .address_space:  global
        .offset:         0
        .size:           8
        .value_kind:     global_buffer
      - .actual_access:  read_only
        .address_space:  global
        .offset:         8
        .size:           8
        .value_kind:     global_buffer
      - .actual_access:  write_only
        .address_space:  global
        .offset:         16
        .size:           8
        .value_kind:     global_buffer
    .group_segment_fixed_size: 66580
    .kernarg_segment_align: 8
    .kernarg_segment_size: 24
    .language:       OpenCL C
    .language_version:
      - 2
      - 0
    .max_flat_workgroup_size: 320
    .name:           _Z7k_att1nPKDF16_S0_Pf
    .private_segment_fixed_size: 0
    .sgpr_count:     29
    .sgpr_spill_count: 0
    .symbol:         _Z7k_att1nPKDF16_S0_Pf.kd
    .uniform_work_group_size: 1
    .uses_dynamic_stack: false
    .vgpr_count:     126
    .vgpr_spill_count: 0
    .wavefront_size: 64
  - .agpr_count:     0
    .args:
      - .actual_access:  read_only
        .address_space:  global
        .offset:         0
        .size:           8
        .value_kind:     global_buffer
      - .actual_access:  read_only
        .address_space:  global
        .offset:         8
        .size:           8
        .value_kind:     global_buffer
      - .actual_access:  read_only
        .address_space:  global
        .offset:         16
        .size:           8
        .value_kind:     global_buffer
      - .actual_access:  write_only
        .address_space:  global
        .offset:         24
        .size:           8
        .value_kind:     global_buffer
      - .actual_access:  read_only
        .address_space:  global
        .offset:         32
        .size:           8
        .value_kind:     global_buffer
      - .actual_access:  read_only
        .address_space:  global
        .offset:         40
        .size:           8
        .value_kind:     global_buffer
      - .actual_access:  read_only
        .address_space:  global
        .offset:         48
        .size:           8
        .value_kind:     global_buffer
      - .actual_access:  read_only
        .address_space:  global
        .offset:         56
        .size:           8
        .value_kind:     global_buffer
      - .actual_access:  read_only
        .address_space:  global
        .offset:         64
        .size:           8
        .value_kind:     global_buffer
      - .actual_access:  read_only
        .address_space:  global
        .offset:         72
        .size:           8
        .value_kind:     global_buffer
      - .actual_access:  read_only
        .address_space:  global
        .offset:         80
        .size:           8
        .value_kind:     global_buffer
      - .actual_access:  read_only
        .address_space:  global
        .offset:         88
        .size:           8
        .value_kind:     global_buffer
      - .actual_access:  read_only
        .address_space:  global
        .offset:         96
        .size:           8
        .value_kind:     global_buffer
      - .actual_access:  write_only
        .address_space:  global
        .offset:         104
        .size:           8
        .value_kind:     global_buffer
    .group_segment_fixed_size: 70720
    .kernarg_segment_align: 8
    .kernarg_segment_size: 112
    .language:       OpenCL C
    .language_version:
      - 2
      - 0
    .max_flat_workgroup_size: 320
    .name:           _Z7k_att2nPKDF16_S0_PKfPfS2_S2_S2_S2_S2_S2_S2_S2_S2_S3_
    .private_segment_fixed_size: 0
    .sgpr_count:     58
    .sgpr_spill_count: 0
    .symbol:         _Z7k_att2nPKDF16_S0_PKfPfS2_S2_S2_S2_S2_S2_S2_S2_S2_S3_.kd
    .uniform_work_group_size: 1
    .uses_dynamic_stack: false
    .vgpr_count:     122
    .vgpr_spill_count: 0
    .wavefront_size: 64
  - .agpr_count:     0
    .args:
      - .actual_access:  read_only
        .address_space:  global
        .offset:         0
        .size:           8
        .value_kind:     global_buffer
      - .actual_access:  read_only
        .address_space:  global
        .offset:         8
        .size:           8
        .value_kind:     global_buffer
      - .actual_access:  read_only
        .address_space:  global
        .offset:         16
        .size:           8
        .value_kind:     global_buffer
      - .actual_access:  read_only
        .address_space:  global
        .offset:         24
        .size:           8
        .value_kind:     global_buffer
      - .actual_access:  read_only
        .address_space:  global
        .offset:         32
        .size:           8
        .value_kind:     global_buffer
      - .actual_access:  read_only
        .address_space:  global
        .offset:         40
        .size:           8
        .value_kind:     global_buffer
      - .actual_access:  read_only
        .address_space:  global
        .offset:         48
        .size:           8
        .value_kind:     global_buffer
      - .actual_access:  read_only
        .address_space:  global
        .offset:         56
        .size:           8
        .value_kind:     global_buffer
      - .actual_access:  read_only
        .address_space:  global
        .offset:         64
        .size:           8
        .value_kind:     global_buffer
      - .actual_access:  write_only
        .address_space:  global
        .offset:         72
        .size:           8
        .value_kind:     global_buffer
    .group_segment_fixed_size: 704
    .kernarg_segment_align: 8
    .kernarg_segment_size: 80
    .language:       OpenCL C
    .language_version:
      - 2
      - 0
    .max_flat_workgroup_size: 64
    .name:           _Z8k_heads3PKfS0_S0_S0_S0_S0_S0_S0_S0_Pf
    .private_segment_fixed_size: 0
    .sgpr_count:     24
    .sgpr_spill_count: 0
    .symbol:         _Z8k_heads3PKfS0_S0_S0_S0_S0_S0_S0_S0_Pf.kd
    .uniform_work_group_size: 1
    .uses_dynamic_stack: false
    .vgpr_count:     121
    .vgpr_spill_count: 0
    .wavefront_size: 64
